# speedup vs baseline: 1.0131x; 1.0019x over previous
.LBB13_3:
	s_load_dwordx2 s[2:3], s[0:1], 0x58
	s_load_dwordx4 s[4:7], s[0:1], 0x48
	s_load_dwordx2 s[22:23], s[0:1], 0x0
	s_load_dwordx2 s[24:25], s[0:1], 0x18
	s_load_dwordx2 s[18:19], s[0:1], 0x30
	s_load_dwordx2 s[0:1], s[0:1], 0x8
	s_andn2_b64 vcc, exec, s[26:27]
	s_cbranch_vccnz .LBB13_5
	s_abs_i32 s17, s16
	v_cvt_f32_u32_e32 v4, s17
	s_ashr_i32 s16, s16, 31
	v_xor_b32_e32 v5, s16, v3
	s_sub_i32 s16, 0, s17
	v_rcp_iflag_f32_e32 v4, v4
	v_max_i32_e32 v1, v2, v1
	v_mul_f32_e32 v4, 0x4f7ffffe, v4
	v_cvt_u32_f32_e32 v4, v4
	v_mul_lo_u32 v6, s16, v4
	v_mul_hi_u32 v6, v4, v6
	v_add_u32_e32 v4, v4, v6
	v_mul_hi_u32 v4, v1, v4
	v_mul_lo_u32 v6, v4, s17
	v_sub_u32_e32 v1, v1, v6
	v_add_u32_e32 v7, 1, v4
	v_cmp_le_u32_e32 vcc, s17, v1
	v_subrev_u32_e32 v6, s17, v1
	s_nop 0
	v_cndmask_b32_e32 v4, v4, v7, vcc
	v_cndmask_b32_e32 v1, v1, v6, vcc
	v_add_u32_e32 v6, 1, v4
	v_cmp_le_u32_e32 vcc, s17, v1
	s_nop 1
	v_cndmask_b32_e32 v4, v4, v6, vcc
	v_xor_b32_e32 v4, v4, v5
	v_sub_u32_e32 v6, v4, v5
	v_subrev_u32_e32 v4, s17, v1
	v_cndmask_b32_e32 v1, v1, v4, vcc
	v_xor_b32_e32 v1, v1, v3
	v_sub_u32_e32 v4, v1, v3
	v_ashrrev_i32_e32 v5, 31, v4
	v_ashrrev_i32_e32 v7, 31, v6
	v_mad_i64_i32 v[4:5], s[16:17], v6, 17, v[4:5]
.LBB13_5:
	v_lshlrev_b32_e32 v0, 2, v0
	v_and_b32_e32 v58, 0xfc, v0
	v_lshlrev_b64 v[4:5], 11, v[4:5]
	v_lshlrev_b32_e32 v0, 2, v58
	v_mov_b32_e32 v1, 0
	s_waitcnt lgkmcnt(0)
	v_lshl_add_u64 v[4:5], s[24:25], 0, v[4:5]
	v_lshl_add_u64 v[4:5], v[4:5], 0, v[0:1]
	global_load_dwordx4 v[8:11], v[4:5], off
	global_load_dwordx4 v[12:15], v0, s[20:21]
	global_load_dwordx4 v[16:19], v0, s[20:21] offset:1024
	global_load_dwordx4 v[20:23], v[4:5], off offset:1024
	v_lshlrev_b64 v[4:5], 11, v[2:3]
	v_lshl_add_u64 v[32:33], s[22:23], 0, v[4:5]
	v_lshl_add_u64 v[34:35], v[32:33], 0, v[0:1]
	v_lshl_add_u64 v[32:33], s[0:1], 2, v[32:33]
	global_load_dwordx4 v[24:27], v[34:35], off
	global_load_dwordx4 v[28:31], v[34:35], off offset:1024
	v_lshl_add_u64 v[40:41], v[32:33], 0, v[0:1]
	global_load_dwordx4 v[32:35], v[40:41], off
	global_load_dwordx4 v[36:39], v[40:41], off offset:1024
	global_load_dwordx4 v[44:47], v0, s[12:13] offset:1024
	v_lshlrev_b64 v[6:7], 11, v[6:7]
	global_load_dwordx4 v[40:43], v0, s[12:13]
	v_lshl_add_u64 v[6:7], s[18:19], 0, v[6:7]
	global_load_dwordx4 v[48:51], v0, s[14:15]
	v_lshl_add_u64 v[52:53], v[6:7], 0, v[0:1]
	v_mov_b32_e32 v59, 0x3727c5ac
	s_mov_b32 s12, 0xf800000
	v_mov_b32_e32 v60, 0x260
	v_lshl_add_u64 v[4:5], s[4:5], 0, v[4:5]
	v_lshlrev_b64 v[2:3], 10, v[2:3]
	s_waitcnt vmcnt(9)
	v_pk_add_f32 v[54:55], v[12:13], v[8:9]
	v_pk_add_f32 v[56:57], v[14:15], v[10:11]
	s_waitcnt vmcnt(7)
	v_pk_add_f32 v[20:21], v[16:17], v[20:21]
	v_pk_add_f32 v[18:19], v[18:19], v[22:23]
	global_load_dwordx4 v[6:9], v0, s[8:9]
	global_load_dwordx4 v[10:13], v0, s[10:11]
	global_load_dwordx4 v[14:17], v0, s[14:15] offset:1024
	s_waitcnt vmcnt(9)
	v_pk_add_f32 v[54:55], v[54:55], v[24:25]
	v_pk_add_f32 v[26:27], v[56:57], v[26:27]
	s_waitcnt vmcnt(8)
	v_pk_add_f32 v[28:29], v[20:21], v[28:29]
	v_pk_add_f32 v[30:31], v[18:19], v[30:31]
	global_load_dwordx4 v[18:21], v0, s[8:9] offset:1024
	global_load_dwordx4 v[22:25], v0, s[10:11] offset:1024
	s_waitcnt vmcnt(9)
	v_pk_add_f32 v[54:55], v[54:55], v[32:33]
	v_pk_add_f32 v[34:35], v[26:27], v[34:35]
	s_waitcnt vmcnt(8)
	v_pk_add_f32 v[36:37], v[28:29], v[36:37]
	v_pk_add_f32 v[38:39], v[30:31], v[38:39]
	global_load_dwordx4 v[26:29], v[52:53], off
	global_load_dwordx4 v[30:33], v[52:53], off offset:1024
	v_add_f32_e32 v52, 0, v54
	v_add_f32_e32 v52, v52, v55
	v_add_f32_e32 v52, v52, v34
	v_add_f32_e32 v52, v52, v35
	v_add_f32_e32 v52, v52, v36
	v_add_f32_e32 v52, v52, v37
	v_add_f32_e32 v52, v52, v38
	v_add_f32_e32 v52, v52, v39
	s_nop 1
	v_add_f32_dpp v52, v52, v52 quad_perm:[1,0,3,2] row_mask:0xf bank_mask:0xf bound_ctrl:1
	s_nop 1
	v_add_f32_dpp v52, v52, v52 quad_perm:[2,3,0,1] row_mask:0xf bank_mask:0xf bound_ctrl:1
	s_nop 1
	v_add_f32_dpp v52, v52, v52 row_half_mirror row_mask:0xf bank_mask:0xf bound_ctrl:1
	s_nop 1
	v_add_f32_dpp v52, v52, v52 row_mirror row_mask:0xf bank_mask:0xf bound_ctrl:1
	s_nop 0
	v_readlane_b32 s8, v52, 16
	v_readlane_b32 s9, v52, 48
	v_readlane_b32 s0, v52, 0
	v_readlane_b32 s1, v52, 32
	v_mov_b32_e32 v52, s8
	v_mov_b32_e32 v53, s9
	v_pk_add_f32 v[52:53], s[0:1], v[52:53]
	s_nop 0
	v_add_f32_e32 v52, v52, v53
	v_mul_f32_e32 v52, 0x3b000000, v52
	v_pk_add_f32 v[54:55], v[54:55], v[52:53] op_sel_hi:[1,0] neg_lo:[0,1] neg_hi:[0,1]
	v_pk_add_f32 v[34:35], v[34:35], v[52:53] op_sel_hi:[1,0] neg_lo:[0,1] neg_hi:[0,1]
	v_pk_add_f32 v[36:37], v[36:37], v[52:53] op_sel_hi:[1,0] neg_lo:[0,1] neg_hi:[0,1]
	v_pk_add_f32 v[38:39], v[38:39], v[52:53] op_sel_hi:[1,0] neg_lo:[0,1] neg_hi:[0,1]
	v_pk_mul_f32 v[52:53], v[54:55], v[54:55]
	s_waitcnt vmcnt(8)
	v_pk_mul_f32 v[40:41], v[40:41], v[54:55]
	v_add_f32_e32 v56, v52, v53
	v_pk_mul_f32 v[52:53], v[34:35], v[34:35]
	v_pk_mul_f32 v[34:35], v[42:43], v[34:35]
	v_add_f32_e32 v52, v56, v52
	v_add_f32_e32 v56, v52, v53
	v_pk_mul_f32 v[52:53], v[36:37], v[36:37]
	v_pk_mul_f32 v[36:37], v[44:45], v[36:37]
	v_add_f32_e32 v52, v56, v52
	v_add_f32_e32 v56, v52, v53
	v_pk_mul_f32 v[52:53], v[38:39], v[38:39]
	v_pk_mul_f32 v[38:39], v[46:47], v[38:39]
	v_add_f32_e32 v52, v56, v52
	v_add_f32_e32 v52, v52, v53
	s_nop 1
	v_add_f32_dpp v52, v52, v52 quad_perm:[1,0,3,2] row_mask:0xf bank_mask:0xf bound_ctrl:1
	s_nop 1
	v_add_f32_dpp v52, v52, v52 quad_perm:[2,3,0,1] row_mask:0xf bank_mask:0xf bound_ctrl:1
	s_nop 1
	v_add_f32_dpp v52, v52, v52 row_half_mirror row_mask:0xf bank_mask:0xf bound_ctrl:1
	s_nop 1
	v_add_f32_dpp v52, v52, v52 row_mirror row_mask:0xf bank_mask:0xf bound_ctrl:1
	s_nop 0
	v_readlane_b32 s8, v52, 16
	v_readlane_b32 s9, v52, 48
	v_readlane_b32 s0, v52, 0
	v_readlane_b32 s1, v52, 32
	v_mov_b32_e32 v52, s8
	v_mov_b32_e32 v53, s9
	v_pk_add_f32 v[52:53], s[0:1], v[52:53]
	s_nop 0
	v_add_f32_e32 v52, v52, v53
	v_fmamk_f32 v52, v52, 0x3b000000, v59
	v_mul_f32_e32 v53, 0x4f800000, v52
	v_cmp_gt_f32_e32 vcc, s12, v52
	s_nop 1
	v_cndmask_b32_e32 v52, v52, v53, vcc
	v_sqrt_f32_e32 v53, v52
	s_nop 0
	v_add_u32_e32 v42, -1, v53
	v_add_u32_e32 v43, 1, v53
	v_fma_f32 v44, -v42, v53, v52
	v_fma_f32 v45, -v43, v53, v52
	v_cmp_ge_f32_e64 s[0:1], 0, v44
	s_nop 1
	v_cndmask_b32_e64 v42, v53, v42, s[0:1]
	v_cmp_lt_f32_e64 s[0:1], 0, v45
	s_nop 1
	v_cndmask_b32_e64 v42, v42, v43, s[0:1]
	v_mul_f32_e32 v43, 0x37800000, v42
	v_cndmask_b32_e32 v42, v42, v43, vcc
	v_cmp_class_f32_e32 vcc, v52, v60
	s_nop 1
	v_cndmask_b32_e32 v42, v42, v52, vcc
	v_div_scale_f32 v43, s[0:1], v42, v42, 1.0
	v_rcp_f32_e32 v44, v43
	v_div_scale_f32 v45, vcc, 1.0, v42, 1.0
	v_fma_f32 v46, -v43, v44, 1.0
	v_fmac_f32_e32 v44, v46, v44
	v_mul_f32_e32 v46, v45, v44
	v_fma_f32 v47, -v43, v46, v45
	v_fmac_f32_e32 v46, v47, v44
	v_fma_f32 v43, -v43, v46, v45
	v_div_fmas_f32 v43, v43, v44, v46
	v_div_fixup_f32 v42, v43, v42, 1.0
	s_waitcnt vmcnt(7)
	v_pk_fma_f32 v[40:41], v[42:43], v[40:41], v[48:49] op_sel_hi:[0,1,1]
	s_waitcnt vmcnt(4)
	v_pk_fma_f32 v[14:15], v[42:43], v[36:37], v[14:15] op_sel_hi:[0,1,1]
	s_waitcnt vmcnt(1)
	v_pk_add_f32 v[26:27], v[40:41], v[26:27]
	v_pk_fma_f32 v[34:35], v[42:43], v[34:35], v[50:51] op_sel_hi:[0,1,1]
	s_waitcnt vmcnt(0)
	v_pk_add_f32 v[14:15], v[14:15], v[30:31]
	v_add_f32_e32 v30, 0, v26
	v_pk_add_f32 v[28:29], v[34:35], v[28:29]
	v_add_f32_e32 v30, v30, v27
	v_add_f32_e32 v30, v30, v28
	v_add_f32_e32 v30, v30, v29
	v_pk_fma_f32 v[16:17], v[42:43], v[38:39], v[16:17] op_sel_hi:[0,1,1]
	v_add_f32_e32 v30, v30, v14
	v_pk_add_f32 v[16:17], v[16:17], v[32:33]
	v_add_f32_e32 v30, v30, v15
	v_add_f32_e32 v30, v30, v16
	v_add_f32_e32 v30, v30, v17
	s_nop 1
	v_add_f32_dpp v30, v30, v30 quad_perm:[1,0,3,2] row_mask:0xf bank_mask:0xf bound_ctrl:1
	s_nop 1
	v_add_f32_dpp v30, v30, v30 quad_perm:[2,3,0,1] row_mask:0xf bank_mask:0xf bound_ctrl:1
	s_nop 1
	v_add_f32_dpp v30, v30, v30 row_half_mirror row_mask:0xf bank_mask:0xf bound_ctrl:1
	s_nop 1
	v_add_f32_dpp v30, v30, v30 row_mirror row_mask:0xf bank_mask:0xf bound_ctrl:1
	s_nop 0
	v_readlane_b32 s8, v30, 16
	v_readlane_b32 s9, v30, 48
	v_readlane_b32 s0, v30, 0
	v_readlane_b32 s1, v30, 32
	v_mov_b32_e32 v30, s8
	v_mov_b32_e32 v31, s9
	v_pk_add_f32 v[30:31], s[0:1], v[30:31]
	s_nop 0
	v_add_f32_e32 v30, v30, v31
	v_mul_f32_e32 v30, 0x3b000000, v30
	v_pk_add_f32 v[26:27], v[26:27], v[30:31] op_sel_hi:[1,0] neg_lo:[0,1] neg_hi:[0,1]
	v_pk_add_f32 v[28:29], v[28:29], v[30:31] op_sel_hi:[1,0] neg_lo:[0,1] neg_hi:[0,1]
	v_pk_add_f32 v[14:15], v[14:15], v[30:31] op_sel_hi:[1,0] neg_lo:[0,1] neg_hi:[0,1]
	v_pk_add_f32 v[16:17], v[16:17], v[30:31] op_sel_hi:[1,0] neg_lo:[0,1] neg_hi:[0,1]
	v_pk_mul_f32 v[30:31], v[26:27], v[26:27]
	v_pk_mul_f32 v[32:33], v[28:29], v[28:29]
	v_add_f32_e32 v30, v30, v31
	v_add_f32_e32 v30, v30, v32
	v_pk_mul_f32 v[34:35], v[14:15], v[14:15]
	v_add_f32_e32 v30, v30, v33
	v_add_f32_e32 v30, v30, v34
	v_pk_mul_f32 v[36:37], v[16:17], v[16:17]
	v_add_f32_e32 v30, v30, v35
	v_add_f32_e32 v30, v30, v36
	v_add_f32_e32 v30, v30, v37
	s_nop 1
	v_add_f32_dpp v30, v30, v30 quad_perm:[1,0,3,2] row_mask:0xf bank_mask:0xf bound_ctrl:1
	s_nop 1
	v_add_f32_dpp v30, v30, v30 quad_perm:[2,3,0,1] row_mask:0xf bank_mask:0xf bound_ctrl:1
	s_nop 1
	v_add_f32_dpp v30, v30, v30 row_half_mirror row_mask:0xf bank_mask:0xf bound_ctrl:1
	s_nop 1
	v_add_f32_dpp v30, v30, v30 row_mirror row_mask:0xf bank_mask:0xf bound_ctrl:1
	s_nop 0
	v_readlane_b32 s8, v30, 16
	v_readlane_b32 s9, v30, 48
	v_readlane_b32 s0, v30, 0
	v_readlane_b32 s1, v30, 32
	v_mov_b32_e32 v30, s8
	v_mov_b32_e32 v31, s9
	v_pk_add_f32 v[30:31], s[0:1], v[30:31]
	s_nop 0
	v_add_f32_e32 v30, v30, v31
	v_fmac_f32_e32 v59, 0x3b000000, v30
	v_mul_f32_e32 v30, 0x4f800000, v59
	v_cmp_gt_f32_e32 vcc, s12, v59
	s_nop 1
	v_cndmask_b32_e32 v30, v59, v30, vcc
	v_sqrt_f32_e32 v31, v30
	s_nop 0
	v_add_u32_e32 v32, -1, v31
	v_fma_f32 v33, -v32, v31, v30
	v_cmp_ge_f32_e64 s[0:1], 0, v33
	v_add_u32_e32 v33, 1, v31
	s_nop 0
	v_cndmask_b32_e64 v32, v31, v32, s[0:1]
	v_fma_f32 v31, -v33, v31, v30
	v_cmp_lt_f32_e64 s[0:1], 0, v31
	s_nop 1
	v_cndmask_b32_e64 v31, v32, v33, s[0:1]
	v_mul_f32_e32 v32, 0x37800000, v31
	v_cndmask_b32_e32 v31, v31, v32, vcc
	v_cmp_class_f32_e32 vcc, v30, v60
	s_nop 1
	v_cndmask_b32_e32 v32, v31, v30, vcc
	v_div_scale_f32 v33, s[0:1], v32, v32, 1.0
	v_rcp_f32_e32 v34, v33
	v_lshl_add_u64 v[30:31], v[4:5], 0, v[0:1]
	s_mov_b32 s0, 0x43000000
	v_fma_f32 v0, -v33, v34, 1.0
	v_fmac_f32_e32 v34, v0, v34
	v_div_scale_f32 v0, vcc, 1.0, v32, 1.0
	v_mul_f32_e32 v4, v0, v34
	v_fma_f32 v5, -v33, v4, v0
	v_fmac_f32_e32 v4, v5, v34
	v_fma_f32 v0, -v33, v4, v0
	v_div_fmas_f32 v0, v0, v34, v4
	v_div_fixup_f32 v0, v0, v32, 1.0
	v_pk_mul_f32 v[4:5], v[6:7], v[26:27]
	v_pk_mul_f32 v[6:7], v[8:9], v[28:29]
	v_pk_fma_f32 v[4:5], v[0:1], v[4:5], v[10:11] op_sel_hi:[0,1,1]
	v_pk_mul_f32 v[8:9], v[18:19], v[14:15]
	v_pk_fma_f32 v[6:7], v[0:1], v[6:7], v[12:13] op_sel_hi:[0,1,1]
	v_pk_fma_f32 v[8:9], v[0:1], v[8:9], v[22:23] op_sel_hi:[0,1,1]
	v_pk_mul_f32 v[10:11], v[20:21], v[16:17]
	v_fma_mixlo_f16 v12, v4, s0, 0
	v_pk_fma_f32 v[10:11], v[0:1], v[10:11], v[24:25] op_sel_hi:[0,1,1]
	global_store_dwordx4 v[30:31], v[4:7], off sc1
	global_store_dwordx4 v[30:31], v[8:11], off offset:1024 sc1
	v_mul_f32_e32 v0, 0x43000000, v4
	v_fma_mixlo_f16 v4, v4, s0, -v12 op_sel_hi:[0,0,1]
	v_fma_mixlo_f16 v12, v8, s0, 0
	v_mul_f32_e32 v13, 0x43000000, v8
	v_fma_mixlo_f16 v8, v8, s0, -v12 op_sel_hi:[0,0,1]
	v_mul_f32_e32 v12, 0x43000000, v5
	v_fma_mixlo_f16 v14, v5, s0, 0
	v_cvt_pk_f16_f32 v12, v0, v12
	v_mul_f32_e32 v0, 0x43000000, v9
	v_pk_mul_f32 v[16:17], v[6:7], s[0:1] op_sel_hi:[1,0]
	v_fma_mixhi_f16 v4, v5, s0, -v14 op_sel_hi:[0,0,1]
	v_cvt_pk_f16_f32 v14, v13, v0
	v_cvt_pk_f16_f32 v13, v16, v17
	v_pk_mul_f32 v[18:19], v[10:11], s[0:1] op_sel_hi:[1,0]
	v_cvt_f32_f16_e32 v16, v13
	v_cvt_f32_f16_sdwa v17, v13 dst_sel:DWORD dst_unused:UNUSED_PAD src0_sel:WORD_1
	v_cvt_pk_f16_f32 v15, v18, v19
	v_cvt_f32_f16_e32 v18, v15
	v_cvt_f32_f16_sdwa v19, v15 dst_sel:DWORD dst_unused:UNUSED_PAD src0_sel:WORD_1
	v_fma_mixlo_f16 v5, v9, s0, 0
	v_pk_fma_f32 v[6:7], v[6:7], s[0:1], v[16:17] op_sel_hi:[1,0,1] neg_lo:[0,0,1] neg_hi:[0,0,1]
	v_fma_mixhi_f16 v8, v9, s0, -v5 op_sel_hi:[0,0,1]
	v_cvt_pk_f16_f32 v5, v6, v7
	v_pk_fma_f32 v[6:7], v[10:11], s[0:1], v[18:19] op_sel_hi:[1,0,1] neg_lo:[0,0,1] neg_hi:[0,0,1]
	v_lshlrev_b32_e32 v0, 1, v58
	v_cvt_pk_f16_f32 v9, v6, v7
	v_lshl_add_u64 v[6:7], s[6:7], 0, v[2:3]
	v_lshl_add_u64 v[2:3], s[2:3], 0, v[2:3]
	v_lshl_add_u64 v[6:7], v[6:7], 0, v[0:1]
	v_lshl_add_u64 v[0:1], v[2:3], 0, v[0:1]
	global_store_dwordx2 v[6:7], v[12:13], off sc1
	global_store_dwordx2 v[6:7], v[14:15], off offset:512 sc1
	global_store_dwordx2 v[0:1], v[4:5], off sc1
	global_store_dwordx2 v[0:1], v[8:9], off offset:512 sc1
	s_endpgm
	s_endpgm
	s_endpgm
	s_endpgm
	s_endpgm
	s_endpgm
	s_endpgm
	s_endpgm
	s_endpgm
	s_endpgm
	s_endpgm
	s_endpgm
	s_endpgm
	s_endpgm
	s_endpgm
	s_endpgm
	s_endpgm
	s_endpgm
	s_endpgm
	s_endpgm
	s_endpgm
	s_endpgm
	s_endpgm
	s_endpgm
	s_endpgm
	s_endpgm
	s_endpgm

.LBB14_3:
	s_load_dwordx2 s[2:3], s[0:1], 0x58
	s_load_dwordx4 s[4:7], s[0:1], 0x48
	s_load_dwordx2 s[22:23], s[0:1], 0x0
	s_load_dwordx2 s[24:25], s[0:1], 0x18
	s_load_dwordx2 s[18:19], s[0:1], 0x30
	s_load_dwordx2 s[0:1], s[0:1], 0x8
	s_andn2_b64 vcc, exec, s[26:27]
	s_cbranch_vccnz .LBB14_5
	s_abs_i32 s17, s16
	v_cvt_f32_u32_e32 v4, s17
	s_ashr_i32 s16, s16, 31
	v_xor_b32_e32 v5, s16, v3
	s_sub_i32 s16, 0, s17
	v_rcp_iflag_f32_e32 v4, v4
	v_max_i32_e32 v1, v2, v1
	v_mul_f32_e32 v4, 0x4f7ffffe, v4
	v_cvt_u32_f32_e32 v4, v4
	v_mul_lo_u32 v6, s16, v4
	v_mul_hi_u32 v6, v4, v6
	v_add_u32_e32 v4, v4, v6
	v_mul_hi_u32 v4, v1, v4
	v_mul_lo_u32 v6, v4, s17
	v_sub_u32_e32 v1, v1, v6
	v_add_u32_e32 v7, 1, v4
	v_cmp_le_u32_e32 vcc, s17, v1
	v_subrev_u32_e32 v6, s17, v1
	s_nop 0
	v_cndmask_b32_e32 v4, v4, v7, vcc
	v_cndmask_b32_e32 v1, v1, v6, vcc
	v_add_u32_e32 v6, 1, v4
	v_cmp_le_u32_e32 vcc, s17, v1
	s_nop 1
	v_cndmask_b32_e32 v4, v4, v6, vcc
	v_xor_b32_e32 v4, v4, v5
	v_sub_u32_e32 v6, v4, v5
	v_subrev_u32_e32 v4, s17, v1
	v_cndmask_b32_e32 v1, v1, v4, vcc
	v_xor_b32_e32 v1, v1, v3
	v_sub_u32_e32 v4, v1, v3
	v_ashrrev_i32_e32 v5, 31, v4
	v_ashrrev_i32_e32 v7, 31, v6
	v_mad_i64_i32 v[8:9], s[16:17], v6, 17, v[4:5]
.LBB14_5:
	v_lshlrev_b32_e32 v0, 2, v0
	v_and_b32_e32 v60, 0xfc, v0
	v_lshlrev_b64 v[8:9], 11, v[8:9]
	v_lshlrev_b32_e32 v0, 2, v60
	v_mov_b32_e32 v1, 0
	s_waitcnt lgkmcnt(0)
	v_lshl_add_u64 v[8:9], s[24:25], 0, v[8:9]
	v_lshl_add_u64 v[24:25], v[8:9], 0, v[0:1]
	global_load_dwordx4 v[8:11], v[24:25], off
	global_load_dwordx4 v[12:15], v0, s[20:21]
	global_load_dwordx4 v[16:19], v0, s[20:21] offset:1024
	global_load_dwordx4 v[20:23], v[24:25], off offset:1024
	v_lshlrev_b64 v[4:5], 11, v[2:3]
	v_lshl_add_u64 v[36:37], s[22:23], 0, v[4:5]
	v_lshl_add_u64 v[28:29], v[36:37], 0, v[0:1]
	global_load_dwordx4 v[24:27], v[28:29], off
	s_waitcnt lgkmcnt(0)
	v_lshl_add_u64 v[30:31], s[0:1], 2, v[36:37]
	v_lshl_add_u64 v[38:39], v[30:31], 0, v[0:1]
	v_lshl_add_u64 v[32:33], s[0:1], 3, v[36:37]
	v_lshl_add_u64 v[44:45], v[32:33], 0, v[0:1]
	global_load_dwordx4 v[32:35], v[38:39], off
	v_mad_u64_u32 v[48:49], s[16:17], s0, 12, v[36:37]
	global_load_dwordx4 v[28:31], v[28:29], off offset:1024
	v_mov_b32_e32 v40, v49
	v_mad_u64_u32 v[46:47], s[0:1], s1, 12, v[40:41]
	global_load_dwordx4 v[40:43], v[44:45], off
	v_mov_b32_e32 v49, v46
	v_lshl_add_u64 v[56:57], v[48:49], 0, v[0:1]
	global_load_dwordx4 v[36:39], v[38:39], off offset:1024
	v_lshlrev_b64 v[6:7], 11, v[6:7]
	global_load_dwordx4 v[44:47], v[44:45], off offset:1024
	s_nop 0
	global_load_dwordx4 v[48:51], v[56:57], off
	global_load_dwordx4 v[52:55], v[56:57], off offset:1024
	v_lshl_add_u64 v[6:7], s[18:19], 0, v[6:7]
	v_lshl_add_u64 v[56:57], v[6:7], 0, v[0:1]
	v_mov_b32_e32 v61, 0x3727c5ac
	s_mov_b32 s16, 0xf800000
	v_lshl_add_u64 v[4:5], s[4:5], 0, v[4:5]
	v_lshlrev_b64 v[2:3], 10, v[2:3]
	s_waitcnt vmcnt(10)
	v_pk_add_f32 v[58:59], v[12:13], v[8:9]
	v_pk_add_f32 v[14:15], v[14:15], v[10:11]
	global_load_dwordx4 v[6:9], v0, s[12:13]
	global_load_dwordx4 v[10:13], v0, s[14:15]
	s_waitcnt vmcnt(10)
	v_pk_add_f32 v[16:17], v[16:17], v[20:21]
	v_pk_add_f32 v[18:19], v[18:19], v[22:23]
	s_waitcnt vmcnt(9)
	v_pk_add_f32 v[22:23], v[58:59], v[24:25]
	v_pk_add_f32 v[24:25], v[14:15], v[26:27]
	s_waitcnt vmcnt(8)
	v_pk_add_f32 v[32:33], v[22:23], v[32:33]
	v_pk_add_f32 v[34:35], v[24:25], v[34:35]
	s_waitcnt vmcnt(7)
	v_pk_add_f32 v[58:59], v[16:17], v[28:29]
	v_pk_add_f32 v[30:31], v[18:19], v[30:31]
	global_load_dwordx4 v[14:17], v0, s[12:13] offset:1024
	global_load_dwordx4 v[18:21], v0, s[14:15] offset:1024
	global_load_dwordx4 v[22:25], v[56:57], off
	global_load_dwordx4 v[26:29], v[56:57], off offset:1024
	s_waitcnt vmcnt(10)
	v_pk_add_f32 v[32:33], v[32:33], v[40:41]
	v_pk_add_f32 v[34:35], v[34:35], v[42:43]
	s_waitcnt vmcnt(9)
	v_pk_add_f32 v[30:31], v[30:31], v[38:39]
	v_pk_add_f32 v[36:37], v[58:59], v[36:37]
	s_waitcnt vmcnt(7)
	v_pk_add_f32 v[32:33], v[32:33], v[48:49]
	v_pk_add_f32 v[34:35], v[34:35], v[50:51]
	v_add_f32_e32 v38, 0, v32
	v_add_f32_e32 v38, v38, v33
	v_pk_add_f32 v[36:37], v[36:37], v[44:45]
	v_add_f32_e32 v38, v38, v34
	s_waitcnt vmcnt(6)
	v_pk_add_f32 v[36:37], v[36:37], v[52:53]
	v_add_f32_e32 v38, v38, v35
	v_pk_add_f32 v[30:31], v[30:31], v[46:47]
	v_add_f32_e32 v38, v38, v36
	v_pk_add_f32 v[30:31], v[30:31], v[54:55]
	v_add_f32_e32 v38, v38, v37
	v_add_f32_e32 v38, v38, v30
	v_add_f32_e32 v38, v38, v31
	v_mov_b32_e32 v55, 0x260
	s_nop 0
	v_add_f32_dpp v38, v38, v38 quad_perm:[1,0,3,2] row_mask:0xf bank_mask:0xf bound_ctrl:1
	s_nop 1
	v_add_f32_dpp v38, v38, v38 quad_perm:[2,3,0,1] row_mask:0xf bank_mask:0xf bound_ctrl:1
	s_nop 1
	v_add_f32_dpp v38, v38, v38 row_half_mirror row_mask:0xf bank_mask:0xf bound_ctrl:1
	s_nop 1
	v_add_f32_dpp v38, v38, v38 row_mirror row_mask:0xf bank_mask:0xf bound_ctrl:1
	s_nop 0
	v_readlane_b32 s12, v38, 16
	v_readlane_b32 s13, v38, 48
	v_readlane_b32 s0, v38, 0
	v_readlane_b32 s1, v38, 32
	v_mov_b32_e32 v38, s12
	v_mov_b32_e32 v39, s13
	v_pk_add_f32 v[38:39], s[0:1], v[38:39]
	s_nop 0
	v_add_f32_e32 v38, v38, v39
	v_mul_f32_e32 v38, 0x3b000000, v38
	v_pk_add_f32 v[46:47], v[32:33], v[38:39] op_sel_hi:[1,0] neg_lo:[0,1] neg_hi:[0,1]
	v_pk_add_f32 v[48:49], v[34:35], v[38:39] op_sel_hi:[1,0] neg_lo:[0,1] neg_hi:[0,1]
	v_pk_add_f32 v[52:53], v[30:31], v[38:39] op_sel_hi:[1,0] neg_lo:[0,1] neg_hi:[0,1]
	v_pk_mul_f32 v[30:31], v[46:47], v[46:47]
	v_pk_mul_f32 v[32:33], v[48:49], v[48:49]
	v_add_f32_e32 v30, v30, v31
	v_pk_add_f32 v[50:51], v[36:37], v[38:39] op_sel_hi:[1,0] neg_lo:[0,1] neg_hi:[0,1]
	v_add_f32_e32 v30, v30, v32
	v_pk_mul_f32 v[34:35], v[50:51], v[50:51]
	v_add_f32_e32 v30, v30, v33
	v_add_f32_e32 v30, v30, v34
	v_pk_mul_f32 v[36:37], v[52:53], v[52:53]
	v_add_f32_e32 v30, v30, v35
	v_add_f32_e32 v30, v30, v36
	v_add_f32_e32 v30, v30, v37
	s_waitcnt vmcnt(5)
	v_pk_mul_f32 v[6:7], v[6:7], v[46:47]
	v_add_f32_dpp v30, v30, v30 quad_perm:[1,0,3,2] row_mask:0xf bank_mask:0xf bound_ctrl:1
	v_pk_mul_f32 v[8:9], v[8:9], v[48:49]
	s_nop 0
	v_add_f32_dpp v30, v30, v30 quad_perm:[2,3,0,1] row_mask:0xf bank_mask:0xf bound_ctrl:1
	s_nop 1
	v_add_f32_dpp v30, v30, v30 row_half_mirror row_mask:0xf bank_mask:0xf bound_ctrl:1
	s_nop 1
	v_add_f32_dpp v30, v30, v30 row_mirror row_mask:0xf bank_mask:0xf bound_ctrl:1
	s_nop 0
	v_readlane_b32 s12, v30, 16
	v_readlane_b32 s13, v30, 48
	v_readlane_b32 s0, v30, 0
	v_readlane_b32 s1, v30, 32
	v_mov_b32_e32 v30, s12
	v_mov_b32_e32 v31, s13
	v_pk_add_f32 v[30:31], s[0:1], v[30:31]
	s_nop 0
	v_add_f32_e32 v30, v30, v31
	v_fmamk_f32 v30, v30, 0x3b000000, v61
	v_mul_f32_e32 v31, 0x4f800000, v30
	v_cmp_gt_f32_e32 vcc, s16, v30
	s_nop 1
	v_cndmask_b32_e32 v54, v30, v31, vcc
	v_sqrt_f32_e32 v38, v54
	global_load_dwordx4 v[30:33], v0, s[8:9]
	global_load_dwordx4 v[34:37], v0, s[10:11]
	v_add_u32_e32 v39, -1, v38
	v_add_u32_e32 v56, 1, v38
	v_fma_f32 v40, -v39, v38, v54
	v_fma_f32 v41, -v56, v38, v54
	v_cmp_ge_f32_e64 s[0:1], 0, v40
	s_nop 1
	v_cndmask_b32_e64 v57, v38, v39, s[0:1]
	v_cmp_lt_f32_e64 s[0:1], 0, v41
	global_load_dwordx4 v[38:41], v0, s[8:9] offset:1024
	global_load_dwordx4 v[42:45], v0, s[10:11] offset:1024
	v_cndmask_b32_e64 v46, v57, v56, s[0:1]
	v_mul_f32_e32 v47, 0x37800000, v46
	v_cndmask_b32_e32 v46, v46, v47, vcc
	v_cmp_class_f32_e32 vcc, v54, v55
	s_nop 1
	v_cndmask_b32_e32 v46, v46, v54, vcc
	v_div_scale_f32 v47, s[0:1], v46, v46, 1.0
	v_rcp_f32_e32 v54, v47
	v_div_scale_f32 v48, vcc, 1.0, v46, 1.0
	v_fma_f32 v49, -v47, v54, 1.0
	v_fmac_f32_e32 v54, v49, v54
	v_mul_f32_e32 v49, v48, v54
	v_fma_f32 v56, -v47, v49, v48
	v_fmac_f32_e32 v49, v56, v54
	v_fma_f32 v47, -v47, v49, v48
	v_div_fmas_f32 v47, v47, v54, v49
	v_div_fixup_f32 v46, v47, v46, 1.0
	s_waitcnt vmcnt(8)
	v_pk_fma_f32 v[6:7], v[46:47], v[6:7], v[10:11] op_sel_hi:[0,1,1]
	s_waitcnt vmcnt(5)
	v_pk_add_f32 v[6:7], v[6:7], v[22:23]
	v_pk_fma_f32 v[8:9], v[46:47], v[8:9], v[12:13] op_sel_hi:[0,1,1]
	v_pk_mul_f32 v[10:11], v[14:15], v[50:51]
	v_add_f32_e32 v14, 0, v6
	v_add_f32_e32 v14, v14, v7
	v_pk_add_f32 v[8:9], v[8:9], v[24:25]
	v_pk_fma_f32 v[10:11], v[46:47], v[10:11], v[18:19] op_sel_hi:[0,1,1]
	v_add_f32_e32 v14, v14, v8
	v_pk_mul_f32 v[12:13], v[16:17], v[52:53]
	v_add_f32_e32 v14, v14, v9
	s_waitcnt vmcnt(4)
	v_pk_add_f32 v[10:11], v[10:11], v[26:27]
	v_pk_fma_f32 v[12:13], v[46:47], v[12:13], v[20:21] op_sel_hi:[0,1,1]
	v_add_f32_e32 v14, v14, v10
	v_add_f32_e32 v14, v14, v11
	v_pk_add_f32 v[12:13], v[12:13], v[28:29]
	s_nop 0
	v_add_f32_e32 v14, v14, v12
	v_add_f32_e32 v14, v14, v13
	s_nop 1
	v_add_f32_dpp v14, v14, v14 quad_perm:[1,0,3,2] row_mask:0xf bank_mask:0xf bound_ctrl:1
	s_nop 1
	v_add_f32_dpp v14, v14, v14 quad_perm:[2,3,0,1] row_mask:0xf bank_mask:0xf bound_ctrl:1
	s_nop 1
	v_add_f32_dpp v14, v14, v14 row_half_mirror row_mask:0xf bank_mask:0xf bound_ctrl:1
	s_nop 1
	v_add_f32_dpp v14, v14, v14 row_mirror row_mask:0xf bank_mask:0xf bound_ctrl:1
	s_nop 0
	v_readlane_b32 s8, v14, 16
	v_readlane_b32 s9, v14, 48
	v_readlane_b32 s0, v14, 0
	v_readlane_b32 s1, v14, 32
	v_mov_b32_e32 v14, s8
	v_mov_b32_e32 v15, s9
	v_pk_add_f32 v[14:15], s[0:1], v[14:15]
	s_nop 0
	v_add_f32_e32 v14, v14, v15
	v_mul_f32_e32 v14, 0x3b000000, v14
	v_pk_add_f32 v[6:7], v[6:7], v[14:15] op_sel_hi:[1,0] neg_lo:[0,1] neg_hi:[0,1]
	v_pk_add_f32 v[8:9], v[8:9], v[14:15] op_sel_hi:[1,0] neg_lo:[0,1] neg_hi:[0,1]
	v_pk_mul_f32 v[16:17], v[6:7], v[6:7]
	v_pk_mul_f32 v[18:19], v[8:9], v[8:9]
	v_add_f32_e32 v16, v16, v17
	v_pk_add_f32 v[10:11], v[10:11], v[14:15] op_sel_hi:[1,0] neg_lo:[0,1] neg_hi:[0,1]
	v_add_f32_e32 v16, v16, v18
	v_pk_mul_f32 v[20:21], v[10:11], v[10:11]
	v_add_f32_e32 v16, v16, v19
	v_pk_add_f32 v[12:13], v[12:13], v[14:15] op_sel_hi:[1,0] neg_lo:[0,1] neg_hi:[0,1]
	v_add_f32_e32 v16, v16, v20
	v_pk_mul_f32 v[14:15], v[12:13], v[12:13]
	v_add_f32_e32 v16, v16, v21
	v_add_f32_e32 v14, v16, v14
	v_add_f32_e32 v14, v14, v15
	s_nop 1
	v_add_f32_dpp v14, v14, v14 quad_perm:[1,0,3,2] row_mask:0xf bank_mask:0xf bound_ctrl:1
	s_nop 1
	v_add_f32_dpp v14, v14, v14 quad_perm:[2,3,0,1] row_mask:0xf bank_mask:0xf bound_ctrl:1
	s_nop 1
	v_add_f32_dpp v14, v14, v14 row_half_mirror row_mask:0xf bank_mask:0xf bound_ctrl:1
	s_nop 1
	v_add_f32_dpp v14, v14, v14 row_mirror row_mask:0xf bank_mask:0xf bound_ctrl:1
	s_nop 0
	v_readlane_b32 s8, v14, 16
	v_readlane_b32 s9, v14, 48
	v_readlane_b32 s0, v14, 0
	v_readlane_b32 s1, v14, 32
	v_mov_b32_e32 v14, s8
	v_mov_b32_e32 v15, s9
	v_pk_add_f32 v[14:15], s[0:1], v[14:15]
	s_nop 0
	v_add_f32_e32 v14, v14, v15
	v_fmac_f32_e32 v61, 0x3b000000, v14
	v_mul_f32_e32 v14, 0x4f800000, v61
	v_cmp_gt_f32_e32 vcc, s16, v61
	s_nop 1
	v_cndmask_b32_e32 v14, v61, v14, vcc
	v_sqrt_f32_e32 v15, v14
	s_nop 0
	v_add_u32_e32 v16, -1, v15
	v_fma_f32 v17, -v16, v15, v14
	v_cmp_ge_f32_e64 s[0:1], 0, v17
	v_add_u32_e32 v17, 1, v15
	s_nop 0
	v_cndmask_b32_e64 v16, v15, v16, s[0:1]
	v_fma_f32 v15, -v17, v15, v14
	v_cmp_lt_f32_e64 s[0:1], 0, v15
	s_nop 1
	v_cndmask_b32_e64 v15, v16, v17, s[0:1]
	v_mul_f32_e32 v16, 0x37800000, v15
	v_cndmask_b32_e32 v15, v15, v16, vcc
	v_cmp_class_f32_e32 vcc, v14, v55
	s_nop 1
	v_cndmask_b32_e32 v16, v15, v14, vcc
	v_div_scale_f32 v17, s[0:1], v16, v16, 1.0
	v_rcp_f32_e32 v18, v17
	v_lshl_add_u64 v[14:15], v[4:5], 0, v[0:1]
	s_mov_b32 s0, 0x43000000
	v_fma_f32 v0, -v17, v18, 1.0
	v_fmac_f32_e32 v18, v0, v18
	v_div_scale_f32 v0, vcc, 1.0, v16, 1.0
	v_mul_f32_e32 v4, v0, v18
	v_fma_f32 v5, -v17, v4, v0
	v_fmac_f32_e32 v4, v5, v18
	v_fma_f32 v0, -v17, v4, v0
	v_div_fmas_f32 v0, v0, v18, v4
	v_div_fixup_f32 v0, v0, v16, 1.0
	s_waitcnt vmcnt(3)
	v_pk_mul_f32 v[4:5], v[30:31], v[6:7]
	v_pk_mul_f32 v[6:7], v[32:33], v[8:9]
	s_waitcnt vmcnt(2)
	v_pk_fma_f32 v[4:5], v[0:1], v[4:5], v[34:35] op_sel_hi:[0,1,1]
	s_waitcnt vmcnt(1)
	v_pk_mul_f32 v[8:9], v[38:39], v[10:11]
	v_pk_fma_f32 v[6:7], v[0:1], v[6:7], v[36:37] op_sel_hi:[0,1,1]
	s_waitcnt vmcnt(0)
	v_pk_fma_f32 v[8:9], v[0:1], v[8:9], v[42:43] op_sel_hi:[0,1,1]
	v_pk_mul_f32 v[10:11], v[40:41], v[12:13]
	v_fma_mixlo_f16 v12, v4, s0, 0
	v_pk_fma_f32 v[10:11], v[0:1], v[10:11], v[44:45] op_sel_hi:[0,1,1]
	global_store_dwordx4 v[14:15], v[4:7], off sc1
	global_store_dwordx4 v[14:15], v[8:11], off offset:1024 sc1
	v_mul_f32_e32 v0, 0x43000000, v4
	v_fma_mixlo_f16 v4, v4, s0, -v12 op_sel_hi:[0,0,1]
	v_fma_mixlo_f16 v12, v8, s0, 0
	v_mul_f32_e32 v13, 0x43000000, v8
	v_fma_mixlo_f16 v8, v8, s0, -v12 op_sel_hi:[0,0,1]
	v_mul_f32_e32 v12, 0x43000000, v5
	v_fma_mixlo_f16 v14, v5, s0, 0
	v_cvt_pk_f16_f32 v12, v0, v12
	v_mul_f32_e32 v0, 0x43000000, v9
	v_pk_mul_f32 v[16:17], v[6:7], s[0:1] op_sel_hi:[1,0]
	v_fma_mixhi_f16 v4, v5, s0, -v14 op_sel_hi:[0,0,1]
	v_cvt_pk_f16_f32 v14, v13, v0
	v_cvt_pk_f16_f32 v13, v16, v17
	v_pk_mul_f32 v[18:19], v[10:11], s[0:1] op_sel_hi:[1,0]
	v_cvt_f32_f16_e32 v16, v13
	v_cvt_f32_f16_sdwa v17, v13 dst_sel:DWORD dst_unused:UNUSED_PAD src0_sel:WORD_1
	v_cvt_pk_f16_f32 v15, v18, v19
	v_cvt_f32_f16_e32 v18, v15
	v_cvt_f32_f16_sdwa v19, v15 dst_sel:DWORD dst_unused:UNUSED_PAD src0_sel:WORD_1
	v_fma_mixlo_f16 v5, v9, s0, 0
	v_pk_fma_f32 v[6:7], v[6:7], s[0:1], v[16:17] op_sel_hi:[1,0,1] neg_lo:[0,0,1] neg_hi:[0,0,1]
	v_fma_mixhi_f16 v8, v9, s0, -v5 op_sel_hi:[0,0,1]
	v_cvt_pk_f16_f32 v5, v6, v7
	v_pk_fma_f32 v[6:7], v[10:11], s[0:1], v[18:19] op_sel_hi:[1,0,1] neg_lo:[0,0,1] neg_hi:[0,0,1]
	v_lshlrev_b32_e32 v0, 1, v60
	v_cvt_pk_f16_f32 v9, v6, v7
	v_lshl_add_u64 v[6:7], s[6:7], 0, v[2:3]
	v_lshl_add_u64 v[2:3], s[2:3], 0, v[2:3]
	v_lshl_add_u64 v[6:7], v[6:7], 0, v[0:1]
	v_lshl_add_u64 v[0:1], v[2:3], 0, v[0:1]
	global_store_dwordx2 v[6:7], v[12:13], off sc1
	global_store_dwordx2 v[6:7], v[14:15], off offset:512 sc1
	global_store_dwordx2 v[0:1], v[4:5], off sc1
	global_store_dwordx2 v[0:1], v[8:9], off offset:512 sc1
	s_endpgm
	s_endpgm
	s_endpgm
	s_endpgm
	s_endpgm
	s_endpgm
	s_endpgm
	s_endpgm
	s_endpgm
	s_endpgm
	s_endpgm
	s_endpgm
	s_endpgm
	s_endpgm
	s_endpgm
	s_endpgm
	s_endpgm
	s_endpgm
	s_endpgm
	s_endpgm
	s_endpgm
	s_endpgm
	s_endpgm
	s_endpgm
	s_endpgm
	s_endpgm
	s_endpgm
	s_endpgm
	s_endpgm
	s_endpgm
	s_endpgm
	s_endpgm
	s_endpgm
	s_endpgm
	s_endpgm
	s_endpgm
	s_endpgm
	s_endpgm
	s_endpgm
	s_endpgm
	s_endpgm
	s_endpgm
	s_endpgm
	s_endpgm
	s_endpgm
	s_endpgm
	s_endpgm
	s_endpgm
	s_endpgm

.LBB15_5:
	v_lshlrev_b32_e32 v0, 2, v0
	v_and_b32_e32 v8, 0xfc, v0
	v_lshlrev_b64 v[4:5], 11, v[4:5]
	v_lshlrev_b32_e32 v0, 2, v8
	v_mov_b32_e32 v1, 0
	s_waitcnt lgkmcnt(0)
	v_lshl_add_u64 v[4:5], s[24:25], 0, v[4:5]
	v_lshl_add_u64 v[4:5], v[4:5], 0, v[0:1]
	global_load_dwordx4 v[10:13], v[4:5], off
	global_load_dwordx4 v[14:17], v0, s[20:21]
	global_load_dwordx4 v[18:21], v0, s[20:21] offset:1024
	global_load_dwordx4 v[22:25], v[4:5], off offset:1024
	v_lshlrev_b64 v[4:5], 11, v[2:3]
	v_lshl_add_u64 v[50:51], s[22:23], 0, v[4:5]
	v_lshl_add_u64 v[30:31], v[50:51], 0, v[0:1]
	global_load_dwordx4 v[26:29], v[30:31], off
	s_waitcnt lgkmcnt(0)
	v_lshl_add_u64 v[34:35], s[0:1], 2, v[50:51]
	global_load_dwordx4 v[30:33], v[30:31], off offset:1024
	v_lshl_add_u64 v[42:43], v[34:35], 0, v[0:1]
	global_load_dwordx4 v[34:37], v[42:43], off
	global_load_dwordx4 v[38:41], v[42:43], off offset:1024
	v_lshl_add_u64 v[42:43], s[0:1], 3, v[50:51]
	v_lshl_add_u64 v[52:53], v[42:43], 0, v[0:1]
	global_load_dwordx4 v[42:45], v[52:53], off
	global_load_dwordx4 v[46:49], v[52:53], off offset:1024
	v_mad_u64_u32 v[52:53], s[16:17], s0, 12, v[50:51]
	v_mad_u64_u32 v[56:57], s[16:17], s0, 20, v[50:51]
	v_mad_u64_u32 v[62:63], s[16:17], s0, 24, v[50:51]
	v_lshl_add_u64 v[54:55], s[0:1], 4, v[50:51]
	v_mad_u64_u32 v[50:51], s[16:17], s0, 28, v[50:51]
	v_lshl_add_u64 v[54:55], v[54:55], 0, v[0:1]
	v_lshlrev_b64 v[6:7], 11, v[6:7]
	v_lshl_add_u64 v[6:7], s[18:19], 0, v[6:7]
	v_lshl_add_u64 v[6:7], v[6:7], 0, v[0:1]
	v_lshl_add_u64 v[4:5], s[4:5], 0, v[4:5]
	v_lshlrev_b64 v[2:3], 10, v[2:3]
	s_waitcnt vmcnt(8)
	v_pk_add_f32 v[58:59], v[14:15], v[10:11]
	v_mov_b32_e32 v10, v53
	v_pk_add_f32 v[60:61], v[16:17], v[12:13]
	v_mov_b32_e32 v12, v57
	v_mad_u64_u32 v[10:11], s[16:17], s1, 12, v[10:11]
	v_mov_b32_e32 v53, v10
	v_mov_b32_e32 v10, v63
	v_mad_u64_u32 v[12:13], s[16:17], s1, 20, v[12:13]
	v_mov_b32_e32 v57, v12
	v_mov_b32_e32 v12, v51
	v_mad_u64_u32 v[10:11], s[16:17], s1, 24, v[10:11]
	s_waitcnt vmcnt(6)
	v_pk_add_f32 v[66:67], v[18:19], v[22:23]
	v_lshl_add_u64 v[22:23], v[52:53], 0, v[0:1]
	v_mad_u64_u32 v[64:65], s[0:1], s1, 28, v[12:13]
	v_mov_b32_e32 v63, v10
	v_pk_add_f32 v[68:69], v[20:21], v[24:25]
	global_load_dwordx4 v[10:13], v[54:55], off
	global_load_dwordx4 v[14:17], v[54:55], off offset:1024
	global_load_dwordx4 v[18:21], v[22:23], off
	v_lshl_add_u64 v[52:53], v[56:57], 0, v[0:1]
	s_waitcnt vmcnt(8)
	v_pk_add_f32 v[54:55], v[58:59], v[26:27]
	v_pk_add_f32 v[56:57], v[60:61], v[28:29]
	global_load_dwordx4 v[26:29], v[52:53], off
	v_lshl_add_u64 v[58:59], v[62:63], 0, v[0:1]
	global_load_dwordx4 v[22:25], v[22:23], off offset:1024
	v_mov_b32_e32 v51, v64
	s_waitcnt vmcnt(9)
	v_pk_add_f32 v[60:61], v[66:67], v[30:31]
	v_pk_add_f32 v[62:63], v[68:69], v[32:33]
	s_waitcnt vmcnt(8)
	v_pk_add_f32 v[54:55], v[54:55], v[34:35]
	v_pk_add_f32 v[56:57], v[56:57], v[36:37]
	global_load_dwordx4 v[30:33], v[52:53], off offset:1024
	global_load_dwordx4 v[34:37], v[58:59], off
	v_lshl_add_u64 v[50:51], v[50:51], 0, v[0:1]
	s_waitcnt vmcnt(9)
	v_pk_add_f32 v[52:53], v[60:61], v[38:39]
	v_pk_add_f32 v[60:61], v[62:63], v[40:41]
	s_waitcnt vmcnt(8)
	v_pk_add_f32 v[54:55], v[54:55], v[42:43]
	v_pk_add_f32 v[56:57], v[56:57], v[44:45]
	global_load_dwordx4 v[38:41], v[50:51], off
	global_load_dwordx4 v[42:45], v[58:59], off offset:1024
	s_waitcnt vmcnt(9)
	v_pk_add_f32 v[52:53], v[52:53], v[46:47]
	v_pk_add_f32 v[58:59], v[60:61], v[48:49]
	global_load_dwordx4 v[46:49], v[50:51], off offset:1024
	s_waitcnt vmcnt(7)
	v_pk_add_f32 v[18:19], v[54:55], v[18:19]
	s_nop 0
	v_pk_add_f32 v[10:11], v[18:19], v[10:11]
	v_pk_add_f32 v[20:21], v[56:57], v[20:21]
	v_mov_b32_e32 v57, 0x3727c5ac
	s_waitcnt vmcnt(6)
	v_pk_add_f32 v[18:19], v[10:11], v[26:27]
	v_pk_add_f32 v[12:13], v[20:21], v[12:13]
	s_waitcnt vmcnt(5)
	v_pk_add_f32 v[22:23], v[52:53], v[22:23]
	v_pk_add_f32 v[10:11], v[58:59], v[24:25]
	v_pk_add_f32 v[14:15], v[22:23], v[14:15]
	v_pk_add_f32 v[10:11], v[10:11], v[16:17]
	v_pk_add_f32 v[20:21], v[12:13], v[28:29]
	v_mov_b32_e32 v58, 0x260
	s_waitcnt vmcnt(4)
	v_pk_add_f32 v[50:51], v[14:15], v[30:31]
	v_pk_add_f32 v[52:53], v[10:11], v[32:33]
	global_load_dwordx4 v[10:13], v0, s[12:13]
	global_load_dwordx4 v[14:17], v0, s[14:15]
	s_waitcnt vmcnt(5)
	v_pk_add_f32 v[18:19], v[18:19], v[34:35]
	s_waitcnt vmcnt(4)
	v_pk_add_f32 v[34:35], v[18:19], v[38:39]
	v_pk_add_f32 v[18:19], v[20:21], v[36:37]
	v_add_f32_e32 v9, 0, v34
	v_pk_add_f32 v[36:37], v[18:19], v[40:41]
	global_load_dwordx4 v[18:21], v0, s[12:13] offset:1024
	global_load_dwordx4 v[22:25], v0, s[14:15] offset:1024
	global_load_dwordx4 v[26:29], v[6:7], off
	global_load_dwordx4 v[30:33], v[6:7], off offset:1024
	v_add_f32_e32 v9, v9, v35
	v_add_f32_e32 v9, v9, v36
	s_waitcnt vmcnt(7)
	v_pk_add_f32 v[6:7], v[50:51], v[42:43]
	v_add_f32_e32 v9, v9, v37
	s_waitcnt vmcnt(6)
	v_pk_add_f32 v[6:7], v[6:7], v[46:47]
	v_pk_add_f32 v[38:39], v[52:53], v[44:45]
	v_add_f32_e32 v9, v9, v6
	v_add_f32_e32 v9, v9, v7
	v_pk_add_f32 v[38:39], v[38:39], v[48:49]
	s_nop 0
	v_add_f32_e32 v9, v9, v38
	v_add_f32_e32 v9, v9, v39
	s_nop 1
	v_add_f32_dpp v9, v9, v9 quad_perm:[1,0,3,2] row_mask:0xf bank_mask:0xf bound_ctrl:1
	s_nop 1
	v_add_f32_dpp v9, v9, v9 quad_perm:[2,3,0,1] row_mask:0xf bank_mask:0xf bound_ctrl:1
	s_nop 1
	v_add_f32_dpp v9, v9, v9 row_half_mirror row_mask:0xf bank_mask:0xf bound_ctrl:1
	s_nop 1
	v_add_f32_dpp v9, v9, v9 row_mirror row_mask:0xf bank_mask:0xf bound_ctrl:1
	s_nop 0
	v_readlane_b32 s12, v9, 16
	v_readlane_b32 s13, v9, 48
	v_readlane_b32 s0, v9, 0
	v_readlane_b32 s1, v9, 32
	v_mov_b32_e32 v40, s12
	v_mov_b32_e32 v41, s13
	v_pk_add_f32 v[40:41], s[0:1], v[40:41]
	s_nop 0
	v_add_f32_e32 v9, v40, v41
	v_mul_f32_e32 v40, 0x3b000000, v9
	v_pk_add_f32 v[50:51], v[34:35], v[40:41] op_sel_hi:[1,0] neg_lo:[0,1] neg_hi:[0,1]
	v_pk_add_f32 v[52:53], v[36:37], v[40:41] op_sel_hi:[1,0] neg_lo:[0,1] neg_hi:[0,1]
	v_pk_mul_f32 v[34:35], v[50:51], v[50:51]
	v_pk_mul_f32 v[36:37], v[52:53], v[52:53]
	v_add_f32_e32 v9, v34, v35
	v_pk_add_f32 v[6:7], v[6:7], v[40:41] op_sel_hi:[1,0] neg_lo:[0,1] neg_hi:[0,1]
	v_add_f32_e32 v9, v9, v36
	v_pk_mul_f32 v[42:43], v[6:7], v[6:7]
	v_add_f32_e32 v9, v9, v37
	v_pk_add_f32 v[54:55], v[38:39], v[40:41] op_sel_hi:[1,0] neg_lo:[0,1] neg_hi:[0,1]
	v_add_f32_e32 v9, v9, v42
	v_pk_mul_f32 v[38:39], v[54:55], v[54:55]
	v_add_f32_e32 v9, v9, v43
	v_add_f32_e32 v9, v9, v38
	v_add_f32_e32 v9, v9, v39
	s_waitcnt vmcnt(5)
	v_pk_mul_f32 v[10:11], v[10:11], v[50:51]
	v_add_f32_dpp v9, v9, v9 quad_perm:[1,0,3,2] row_mask:0xf bank_mask:0xf bound_ctrl:1
	v_pk_mul_f32 v[12:13], v[12:13], v[52:53]
	s_waitcnt vmcnt(3)
	v_pk_mul_f32 v[6:7], v[18:19], v[6:7]
	v_add_f32_dpp v9, v9, v9 quad_perm:[2,3,0,1] row_mask:0xf bank_mask:0xf bound_ctrl:1
	s_nop 1
	v_add_f32_dpp v9, v9, v9 row_half_mirror row_mask:0xf bank_mask:0xf bound_ctrl:1
	s_nop 1
	v_add_f32_dpp v9, v9, v9 row_mirror row_mask:0xf bank_mask:0xf bound_ctrl:1
	s_nop 0
	v_readlane_b32 s12, v9, 16
	v_readlane_b32 s13, v9, 48
	v_readlane_b32 s0, v9, 0
	v_readlane_b32 s1, v9, 32
	v_mov_b32_e32 v34, s12
	v_mov_b32_e32 v35, s13
	v_pk_add_f32 v[34:35], s[0:1], v[34:35]
	s_mov_b32 s12, 0xf800000
	v_add_f32_e32 v9, v34, v35
	v_fmamk_f32 v9, v9, 0x3b000000, v57
	v_mul_f32_e32 v34, 0x4f800000, v9
	v_cmp_gt_f32_e32 vcc, s12, v9
	s_nop 1
	v_cndmask_b32_e32 v9, v9, v34, vcc
	v_sqrt_f32_e32 v34, v9
	s_nop 0
	v_add_u32_e32 v35, -1, v34
	v_fma_f32 v36, -v35, v34, v9
	v_cmp_ge_f32_e64 s[0:1], 0, v36
	v_add_u32_e32 v36, 1, v34
	s_nop 0
	v_cndmask_b32_e64 v35, v34, v35, s[0:1]
	v_fma_f32 v34, -v36, v34, v9
	v_cmp_lt_f32_e64 s[0:1], 0, v34
	s_nop 1
	v_cndmask_b32_e64 v34, v35, v36, s[0:1]
	v_mul_f32_e32 v35, 0x37800000, v34
	v_cndmask_b32_e32 v34, v34, v35, vcc
	v_cmp_class_f32_e32 vcc, v9, v58
	s_nop 1
	v_cndmask_b32_e32 v9, v34, v9, vcc
	v_div_scale_f32 v42, s[0:1], v9, v9, 1.0
	v_rcp_f32_e32 v43, v42
	global_load_dwordx4 v[34:37], v0, s[8:9]
	global_load_dwordx4 v[38:41], v0, s[10:11]
	v_fma_f32 v44, -v42, v43, 1.0
	v_fmac_f32_e32 v43, v44, v43
	v_div_scale_f32 v44, vcc, 1.0, v9, 1.0
	v_mul_f32_e32 v45, v44, v43
	v_fma_f32 v46, -v42, v45, v44
	v_fmac_f32_e32 v45, v46, v43
	v_fma_f32 v42, -v42, v45, v44
	v_div_fmas_f32 v56, v42, v43, v45
	global_load_dwordx4 v[42:45], v0, s[8:9] offset:1024
	global_load_dwordx4 v[46:49], v0, s[10:11] offset:1024
	v_div_fixup_f32 v56, v56, v9, 1.0
	v_pk_fma_f32 v[10:11], v[56:57], v[10:11], v[14:15] op_sel_hi:[0,1,1]
	s_waitcnt vmcnt(5)
	v_pk_add_f32 v[10:11], v[10:11], v[26:27]
	v_pk_fma_f32 v[12:13], v[56:57], v[12:13], v[16:17] op_sel_hi:[0,1,1]
	v_add_f32_e32 v9, 0, v10
	v_add_f32_e32 v9, v9, v11
	v_pk_add_f32 v[12:13], v[12:13], v[28:29]
	v_pk_fma_f32 v[6:7], v[56:57], v[6:7], v[22:23] op_sel_hi:[0,1,1]
	v_add_f32_e32 v9, v9, v12
	v_pk_mul_f32 v[14:15], v[20:21], v[54:55]
	v_add_f32_e32 v9, v9, v13
	s_waitcnt vmcnt(4)
	v_pk_add_f32 v[6:7], v[6:7], v[30:31]
	v_pk_fma_f32 v[14:15], v[56:57], v[14:15], v[24:25] op_sel_hi:[0,1,1]
	v_add_f32_e32 v9, v9, v6
	v_add_f32_e32 v9, v9, v7
	v_pk_add_f32 v[14:15], v[14:15], v[32:33]
	s_nop 0
	v_add_f32_e32 v9, v9, v14
	v_add_f32_e32 v9, v9, v15
	s_nop 1
	v_add_f32_dpp v9, v9, v9 quad_perm:[1,0,3,2] row_mask:0xf bank_mask:0xf bound_ctrl:1
	s_nop 1
	v_add_f32_dpp v9, v9, v9 quad_perm:[2,3,0,1] row_mask:0xf bank_mask:0xf bound_ctrl:1
	s_nop 1
	v_add_f32_dpp v9, v9, v9 row_half_mirror row_mask:0xf bank_mask:0xf bound_ctrl:1
	s_nop 1
	v_add_f32_dpp v9, v9, v9 row_mirror row_mask:0xf bank_mask:0xf bound_ctrl:1
	s_nop 0
	v_readlane_b32 s8, v9, 16
	v_readlane_b32 s9, v9, 48
	v_readlane_b32 s0, v9, 0
	v_readlane_b32 s1, v9, 32
	v_mov_b32_e32 v16, s8
	v_mov_b32_e32 v17, s9
	v_pk_add_f32 v[16:17], s[0:1], v[16:17]
	s_nop 0
	v_add_f32_e32 v9, v16, v17
	v_mul_f32_e32 v16, 0x3b000000, v9
	v_pk_add_f32 v[10:11], v[10:11], v[16:17] op_sel_hi:[1,0] neg_lo:[0,1] neg_hi:[0,1]
	v_pk_add_f32 v[12:13], v[12:13], v[16:17] op_sel_hi:[1,0] neg_lo:[0,1] neg_hi:[0,1]
	v_pk_mul_f32 v[18:19], v[10:11], v[10:11]
	v_pk_mul_f32 v[20:21], v[12:13], v[12:13]
	v_add_f32_e32 v9, v18, v19
	v_pk_add_f32 v[22:23], v[6:7], v[16:17] op_sel_hi:[1,0] neg_lo:[0,1] neg_hi:[0,1]
	v_add_f32_e32 v9, v9, v20
	v_pk_mul_f32 v[6:7], v[22:23], v[22:23]
	v_add_f32_e32 v9, v9, v21
	v_pk_add_f32 v[14:15], v[14:15], v[16:17] op_sel_hi:[1,0] neg_lo:[0,1] neg_hi:[0,1]
	v_add_f32_e32 v6, v9, v6
	v_pk_mul_f32 v[16:17], v[14:15], v[14:15]
	v_add_f32_e32 v6, v6, v7
	v_add_f32_e32 v6, v6, v16
	v_add_f32_e32 v6, v6, v17
	s_nop 1
	v_add_f32_dpp v6, v6, v6 quad_perm:[1,0,3,2] row_mask:0xf bank_mask:0xf bound_ctrl:1
	s_nop 1
	v_add_f32_dpp v6, v6, v6 quad_perm:[2,3,0,1] row_mask:0xf bank_mask:0xf bound_ctrl:1
	s_nop 1
	v_add_f32_dpp v6, v6, v6 row_half_mirror row_mask:0xf bank_mask:0xf bound_ctrl:1
	s_nop 1
	v_add_f32_dpp v6, v6, v6 row_mirror row_mask:0xf bank_mask:0xf bound_ctrl:1
	s_nop 0
	v_readlane_b32 s8, v6, 16
	v_readlane_b32 s9, v6, 48
	v_readlane_b32 s0, v6, 0
	v_readlane_b32 s1, v6, 32
	v_mov_b32_e32 v6, s8
	v_mov_b32_e32 v7, s9
	v_pk_add_f32 v[6:7], s[0:1], v[6:7]
	s_nop 0
	v_add_f32_e32 v6, v6, v7
	v_fmac_f32_e32 v57, 0x3b000000, v6
	v_mul_f32_e32 v6, 0x4f800000, v57
	v_cmp_gt_f32_e32 vcc, s12, v57
	s_nop 1
	v_cndmask_b32_e32 v6, v57, v6, vcc
	v_sqrt_f32_e32 v7, v6
	s_nop 0
	v_add_u32_e32 v9, -1, v7
	v_fma_f32 v16, -v9, v7, v6
	v_cmp_ge_f32_e64 s[0:1], 0, v16
	v_add_u32_e32 v16, 1, v7
	s_nop 0
	v_cndmask_b32_e64 v9, v7, v9, s[0:1]
	v_fma_f32 v7, -v16, v7, v6
	v_cmp_lt_f32_e64 s[0:1], 0, v7
	s_nop 1
	v_cndmask_b32_e64 v7, v9, v16, s[0:1]
	v_mul_f32_e32 v9, 0x37800000, v7
	v_cndmask_b32_e32 v7, v7, v9, vcc
	v_cmp_class_f32_e32 vcc, v6, v58
	v_lshl_add_u64 v[16:17], v[4:5], 0, v[0:1]
	s_nop 0
	v_cndmask_b32_e32 v6, v7, v6, vcc
	v_div_scale_f32 v7, s[0:1], v6, v6, 1.0
	v_rcp_f32_e32 v9, v7
	s_mov_b32 s0, 0x43000000
	v_fma_f32 v0, -v7, v9, 1.0
	v_fmac_f32_e32 v9, v0, v9
	v_div_scale_f32 v0, vcc, 1.0, v6, 1.0
	v_mul_f32_e32 v4, v0, v9
	v_fma_f32 v5, -v7, v4, v0
	v_fmac_f32_e32 v4, v5, v9
	v_fma_f32 v0, -v7, v4, v0
	v_div_fmas_f32 v0, v0, v9, v4
	v_div_fixup_f32 v0, v0, v6, 1.0
	s_waitcnt vmcnt(3)
	v_pk_mul_f32 v[4:5], v[34:35], v[10:11]
	v_pk_mul_f32 v[6:7], v[36:37], v[12:13]
	s_waitcnt vmcnt(2)
	v_pk_fma_f32 v[4:5], v[0:1], v[4:5], v[38:39] op_sel_hi:[0,1,1]
	v_pk_fma_f32 v[6:7], v[0:1], v[6:7], v[40:41] op_sel_hi:[0,1,1]
	s_waitcnt vmcnt(1)
	v_pk_mul_f32 v[10:11], v[42:43], v[22:23]
	v_pk_mul_f32 v[12:13], v[44:45], v[14:15]
	v_fma_mixlo_f16 v9, v4, s0, 0
	s_waitcnt vmcnt(0)
	v_pk_fma_f32 v[10:11], v[0:1], v[10:11], v[46:47] op_sel_hi:[0,1,1]
	v_pk_fma_f32 v[12:13], v[0:1], v[12:13], v[48:49] op_sel_hi:[0,1,1]
	global_store_dwordx4 v[16:17], v[4:7], off sc1
	global_store_dwordx4 v[16:17], v[10:13], off offset:1024 sc1
	v_mul_f32_e32 v0, 0x43000000, v4
	v_fma_mixlo_f16 v4, v4, s0, -v9 op_sel_hi:[0,0,1]
	v_fma_mixlo_f16 v15, v5, s0, 0
	v_pk_mul_f32 v[18:19], v[6:7], s[0:1] op_sel_hi:[1,0]
	v_fma_mixhi_f16 v4, v5, s0, -v15 op_sel_hi:[0,0,1]
	v_cvt_pk_f16_f32 v15, v18, v19
	v_pk_mul_f32 v[20:21], v[12:13], s[0:1] op_sel_hi:[1,0]
	v_cvt_f32_f16_e32 v18, v15
	v_cvt_f32_f16_sdwa v19, v15 dst_sel:DWORD dst_unused:UNUSED_PAD src0_sel:WORD_1
	v_cvt_pk_f16_f32 v17, v20, v21
	v_cvt_f32_f16_e32 v20, v17
	v_cvt_f32_f16_sdwa v21, v17 dst_sel:DWORD dst_unused:UNUSED_PAD src0_sel:WORD_1
	v_fma_mixlo_f16 v14, v10, s0, 0
	v_mul_f32_e32 v9, 0x43000000, v10
	v_fma_mixlo_f16 v10, v10, s0, -v14 op_sel_hi:[0,0,1]
	v_mul_f32_e32 v14, 0x43000000, v5
	v_fma_mixlo_f16 v5, v11, s0, 0
	v_pk_fma_f32 v[6:7], v[6:7], s[0:1], v[18:19] op_sel_hi:[1,0,1] neg_lo:[0,0,1] neg_hi:[0,0,1]
	v_cvt_pk_f16_f32 v14, v0, v14
	v_mul_f32_e32 v0, 0x43000000, v11
	v_fma_mixhi_f16 v10, v11, s0, -v5 op_sel_hi:[0,0,1]
	v_cvt_pk_f16_f32 v5, v6, v7
	v_pk_fma_f32 v[6:7], v[12:13], s[0:1], v[20:21] op_sel_hi:[1,0,1] neg_lo:[0,0,1] neg_hi:[0,0,1]
	v_cvt_pk_f16_f32 v16, v9, v0
	v_cvt_pk_f16_f32 v11, v6, v7
	v_lshl_add_u64 v[6:7], s[6:7], 0, v[2:3]
	v_lshlrev_b32_e32 v0, 1, v8
	v_lshl_add_u64 v[2:3], s[2:3], 0, v[2:3]
	v_lshl_add_u64 v[6:7], v[6:7], 0, v[0:1]
	v_lshl_add_u64 v[0:1], v[2:3], 0, v[0:1]
	global_store_dwordx2 v[6:7], v[14:15], off sc1
	global_store_dwordx2 v[6:7], v[16:17], off offset:512 sc1
	global_store_dwordx2 v[0:1], v[4:5], off sc1
	global_store_dwordx2 v[0:1], v[10:11], off offset:512 sc1
	s_endpgm
	s_endpgm
	s_endpgm
	s_endpgm
	s_endpgm
	s_endpgm
	s_endpgm
	s_endpgm
	s_endpgm
	s_endpgm
	s_endpgm
	s_endpgm
	s_endpgm
	s_endpgm
	s_endpgm
	s_endpgm
	s_endpgm
	s_endpgm
	s_endpgm
	s_endpgm
	s_endpgm
	s_endpgm
	s_endpgm
	s_endpgm
	s_endpgm
	s_endpgm
	s_endpgm
	s_endpgm
	s_endpgm

.LBB20_3:
	s_load_dwordx2 s[2:3], s[0:1], 0x58
	s_load_dwordx4 s[4:7], s[0:1], 0x48
	s_load_dwordx2 s[18:19], s[0:1], 0x0
	s_load_dwordx2 s[14:15], s[0:1], 0x18
	s_load_dwordx2 s[0:1], s[0:1], 0x8
	s_andn2_b64 vcc, exec, s[20:21]
	s_cbranch_vccnz .LBB20_5
	s_abs_i32 s13, s12
	v_cvt_f32_u32_e32 v1, s13
	s_sub_i32 s20, 0, s13
	v_sub_u32_e32 v5, 0, v2
	v_max_i32_e32 v5, v2, v5
	v_rcp_iflag_f32_e32 v1, v1
	v_xor_b32_e32 v4, s12, v2
	v_ashrrev_i32_e32 v4, 31, v4
	v_mul_f32_e32 v1, 0x4f7ffffe, v1
	v_cvt_u32_f32_e32 v1, v1
	v_mul_lo_u32 v6, s20, v1
	v_mul_hi_u32 v6, v1, v6
	v_add_u32_e32 v1, v1, v6
	v_mul_hi_u32 v1, v5, v1
	v_mul_lo_u32 v6, v1, s13
	v_sub_u32_e32 v5, v5, v6
	v_add_u32_e32 v7, 1, v1
	v_cmp_le_u32_e32 vcc, s13, v5
	v_subrev_u32_e32 v6, s13, v5
	s_nop 0
	v_cndmask_b32_e32 v1, v1, v7, vcc
	v_cndmask_b32_e32 v5, v5, v6, vcc
	v_add_u32_e32 v6, 1, v1
	v_cmp_le_u32_e32 vcc, s13, v5
	s_nop 1
	v_cndmask_b32_e32 v1, v1, v6, vcc
	v_xor_b32_e32 v1, v1, v4
	v_sub_u32_e32 v1, v1, v4
	v_mul_lo_u32 v4, v1, s12
	v_sub_u32_e32 v4, v2, v4
	v_ashrrev_i32_e32 v5, 31, v4
	v_mad_i64_i32 v[4:5], s[12:13], v1, 17, v[4:5]
.LBB20_5:
	v_lshlrev_b32_e32 v0, 2, v0
	v_and_b32_e32 v54, 0xfc, v0
	v_lshlrev_b64 v[44:45], 11, v[2:3]
	v_lshlrev_b64 v[4:5], 11, v[4:5]
	s_waitcnt lgkmcnt(0)
	v_lshl_add_u64 v[24:25], s[18:19], 0, v[44:45]
	v_lshlrev_b32_e32 v0, 2, v54
	v_mov_b32_e32 v1, 0
	v_lshl_add_u64 v[4:5], s[14:15], 0, v[4:5]
	v_lshl_add_u64 v[20:21], v[4:5], 0, v[0:1]
	v_lshl_add_u64 v[26:27], v[24:25], 0, v[0:1]
	global_load_dwordx4 v[4:7], v[20:21], off
	global_load_dwordx4 v[8:11], v0, s[16:17]
	global_load_dwordx4 v[12:15], v0, s[16:17] offset:1024
	global_load_dwordx4 v[16:19], v[20:21], off offset:1024
	v_lshl_add_u64 v[28:29], s[0:1], 2, v[24:25]
	global_load_dwordx4 v[20:23], v[26:27], off
	v_lshl_add_u64 v[46:47], v[28:29], 0, v[0:1]
	global_load_dwordx4 v[24:27], v[26:27], off offset:1024
	s_nop 0
	global_load_dwordx4 v[28:31], v[46:47], off
	global_load_dwordx4 v[32:35], v[46:47], off offset:1024
	global_load_dwordx4 v[36:39], v0, s[8:9]
	global_load_dwordx4 v[40:43], v0, s[8:9] offset:1024
	v_lshl_add_u64 v[44:45], s[4:5], 0, v[44:45]
	v_lshl_add_u64 v[52:53], v[44:45], 0, v[0:1]
	global_load_dwordx4 v[44:47], v0, s[10:11]
	global_load_dwordx4 v[48:51], v0, s[10:11] offset:1024
	v_mov_b32_e32 v55, 0x3727c5ac
	s_mov_b32 s9, 0xf800000
	v_mov_b32_e32 v56, 0x260
	s_mov_b32 s8, 0x43000000
	v_lshlrev_b64 v[2:3], 10, v[2:3]
	s_waitcnt vmcnt(10)
	v_pk_add_f32 v[4:5], v[8:9], v[4:5]
	v_pk_add_f32 v[6:7], v[10:11], v[6:7]
	s_waitcnt vmcnt(8)
	v_pk_add_f32 v[8:9], v[12:13], v[16:17]
	v_pk_add_f32 v[10:11], v[14:15], v[18:19]
	s_waitcnt vmcnt(7)
	v_pk_add_f32 v[4:5], v[4:5], v[20:21]
	v_pk_add_f32 v[6:7], v[6:7], v[22:23]
	s_waitcnt vmcnt(5)
	v_pk_add_f32 v[4:5], v[4:5], v[28:29]
	v_pk_add_f32 v[6:7], v[6:7], v[30:31]
	v_add_f32_e32 v0, 0, v4
	v_add_f32_e32 v0, v0, v5
	v_pk_add_f32 v[8:9], v[8:9], v[24:25]
	v_add_f32_e32 v0, v0, v6
	s_waitcnt vmcnt(4)
	v_pk_add_f32 v[8:9], v[8:9], v[32:33]
	v_add_f32_e32 v0, v0, v7
	v_pk_add_f32 v[10:11], v[10:11], v[26:27]
	v_add_f32_e32 v0, v0, v8
	v_pk_add_f32 v[10:11], v[10:11], v[34:35]
	v_add_f32_e32 v0, v0, v9
	v_add_f32_e32 v0, v0, v10
	v_add_f32_e32 v0, v0, v11
	s_nop 1
	v_add_f32_dpp v0, v0, v0 quad_perm:[1,0,3,2] row_mask:0xf bank_mask:0xf bound_ctrl:1
	s_nop 1
	v_add_f32_dpp v0, v0, v0 quad_perm:[2,3,0,1] row_mask:0xf bank_mask:0xf bound_ctrl:1
	s_nop 1
	v_add_f32_dpp v0, v0, v0 row_half_mirror row_mask:0xf bank_mask:0xf bound_ctrl:1
	s_nop 1
	v_add_f32_dpp v0, v0, v0 row_mirror row_mask:0xf bank_mask:0xf bound_ctrl:1
	s_nop 0
	v_readlane_b32 s4, v0, 16
	v_readlane_b32 s5, v0, 48
	v_readlane_b32 s0, v0, 0
	v_readlane_b32 s1, v0, 32
	v_mov_b32_e32 v12, s4
	v_mov_b32_e32 v13, s5
	v_pk_add_f32 v[12:13], s[0:1], v[12:13]
	s_nop 0
	v_add_f32_e32 v0, v12, v13
	v_mul_f32_e32 v0, 0x3b000000, v0
	v_pk_add_f32 v[4:5], v[4:5], v[0:1] op_sel_hi:[1,0] neg_lo:[0,1] neg_hi:[0,1]
	v_pk_add_f32 v[6:7], v[6:7], v[0:1] op_sel_hi:[1,0] neg_lo:[0,1] neg_hi:[0,1]
	v_pk_mul_f32 v[12:13], v[4:5], v[4:5]
	v_pk_add_f32 v[8:9], v[8:9], v[0:1] op_sel_hi:[1,0] neg_lo:[0,1] neg_hi:[0,1]
	v_pk_add_f32 v[10:11], v[10:11], v[0:1] op_sel_hi:[1,0] neg_lo:[0,1] neg_hi:[0,1]
	v_pk_mul_f32 v[14:15], v[6:7], v[6:7]
	v_add_f32_e32 v0, v12, v13
	v_add_f32_e32 v0, v0, v14
	v_pk_mul_f32 v[16:17], v[8:9], v[8:9]
	v_add_f32_e32 v0, v0, v15
	v_add_f32_e32 v0, v0, v16
	v_pk_mul_f32 v[18:19], v[10:11], v[10:11]
	v_add_f32_e32 v0, v0, v17
	v_add_f32_e32 v0, v0, v18
	v_add_f32_e32 v0, v0, v19
	s_waitcnt vmcnt(3)
	v_pk_mul_f32 v[6:7], v[38:39], v[6:7]
	s_waitcnt vmcnt(2)
	v_pk_mul_f32 v[8:9], v[40:41], v[8:9]
	v_add_f32_dpp v0, v0, v0 quad_perm:[1,0,3,2] row_mask:0xf bank_mask:0xf bound_ctrl:1
	v_pk_mul_f32 v[4:5], v[36:37], v[4:5]
	v_pk_mul_f32 v[10:11], v[42:43], v[10:11]
	v_add_f32_dpp v0, v0, v0 quad_perm:[2,3,0,1] row_mask:0xf bank_mask:0xf bound_ctrl:1
	s_nop 1
	v_add_f32_dpp v0, v0, v0 row_half_mirror row_mask:0xf bank_mask:0xf bound_ctrl:1
	s_nop 1
	v_add_f32_dpp v0, v0, v0 row_mirror row_mask:0xf bank_mask:0xf bound_ctrl:1
	s_nop 0
	v_readlane_b32 s4, v0, 16
	v_readlane_b32 s5, v0, 48
	v_readlane_b32 s0, v0, 0
	v_readlane_b32 s1, v0, 32
	v_mov_b32_e32 v12, s4
	v_mov_b32_e32 v13, s5
	v_pk_add_f32 v[12:13], s[0:1], v[12:13]
	s_nop 0
	v_add_f32_e32 v0, v12, v13
	v_fmac_f32_e32 v55, 0x3b000000, v0
	v_mul_f32_e32 v0, 0x4f800000, v55
	v_cmp_gt_f32_e32 vcc, s9, v55
	s_nop 1
	v_cndmask_b32_e32 v0, v55, v0, vcc
	v_sqrt_f32_e32 v12, v0
	s_nop 0
	v_add_u32_e32 v13, -1, v12
	v_add_u32_e32 v14, 1, v12
	v_fma_f32 v15, -v13, v12, v0
	v_fma_f32 v16, -v14, v12, v0
	v_cmp_ge_f32_e64 s[0:1], 0, v15
	s_nop 1
	v_cndmask_b32_e64 v12, v12, v13, s[0:1]
	v_cmp_lt_f32_e64 s[0:1], 0, v16
	s_nop 1
	v_cndmask_b32_e64 v12, v12, v14, s[0:1]
	v_mul_f32_e32 v13, 0x37800000, v12
	v_cndmask_b32_e32 v12, v12, v13, vcc
	v_cmp_class_f32_e32 vcc, v0, v56
	s_nop 1
	v_cndmask_b32_e32 v0, v12, v0, vcc
	v_div_scale_f32 v12, s[0:1], v0, v0, 1.0
	v_rcp_f32_e32 v13, v12
	v_div_scale_f32 v14, vcc, 1.0, v0, 1.0
	v_fma_f32 v15, -v12, v13, 1.0
	v_fmac_f32_e32 v13, v15, v13
	v_mul_f32_e32 v15, v14, v13
	v_fma_f32 v16, -v12, v15, v14
	v_fmac_f32_e32 v15, v16, v13
	v_fma_f32 v12, -v12, v15, v14
	v_div_fmas_f32 v12, v12, v13, v15
	v_div_fixup_f32 v0, v12, v0, 1.0
	s_waitcnt vmcnt(1)
	v_pk_fma_f32 v[6:7], v[0:1], v[6:7], v[46:47] op_sel_hi:[0,1,1]
	s_waitcnt vmcnt(0)
	v_pk_fma_f32 v[8:9], v[0:1], v[8:9], v[48:49] op_sel_hi:[0,1,1]
	v_pk_fma_f32 v[4:5], v[0:1], v[4:5], v[44:45] op_sel_hi:[0,1,1]
	v_mul_f32_e32 v17, 0x43000000, v8
	v_fma_mixlo_f16 v18, v8, s8, 0
	v_mul_f32_e32 v21, 0x43000000, v9
	v_pk_mul_f32 v[12:13], v[6:7], s[8:9] op_sel_hi:[1,0]
	v_pk_fma_f32 v[10:11], v[0:1], v[10:11], v[50:51] op_sel_hi:[0,1,1]
	global_store_dwordx4 v[52:53], v[4:7], off sc1
	global_store_dwordx4 v[52:53], v[8:11], off offset:1024 sc1
	v_mul_f32_e32 v0, 0x43000000, v4
	v_fma_mixlo_f16 v16, v4, s8, 0
	v_fma_mixlo_f16 v8, v8, s8, -v18 op_sel_hi:[0,0,1]
	v_cvt_pk_f16_f32 v18, v17, v21
	v_cvt_pk_f16_f32 v17, v12, v13
	v_mul_f32_e32 v19, 0x43000000, v5
	v_pk_mul_f32 v[14:15], v[10:11], s[8:9] op_sel_hi:[1,0]
	v_cvt_f32_f16_e32 v12, v17
	v_cvt_f32_f16_sdwa v13, v17 dst_sel:DWORD dst_unused:UNUSED_PAD src0_sel:WORD_1
	v_fma_mixlo_f16 v4, v4, s8, -v16 op_sel_hi:[0,0,1]
	v_cvt_pk_f16_f32 v16, v0, v19
	v_cvt_pk_f16_f32 v19, v14, v15
	v_cvt_f32_f16_e32 v14, v19
	v_cvt_f32_f16_sdwa v15, v19 dst_sel:DWORD dst_unused:UNUSED_PAD src0_sel:WORD_1
	v_fma_mixlo_f16 v20, v5, s8, 0
	v_pk_fma_f32 v[6:7], v[6:7], s[8:9], v[12:13] op_sel_hi:[1,0,1] neg_lo:[0,0,1] neg_hi:[0,0,1]
	v_fma_mixhi_f16 v4, v5, s8, -v20 op_sel_hi:[0,0,1]
	v_cvt_pk_f16_f32 v5, v6, v7
	v_lshl_add_u64 v[6:7], s[6:7], 0, v[2:3]
	v_lshlrev_b32_e32 v0, 1, v54
	v_lshl_add_u64 v[2:3], s[2:3], 0, v[2:3]
	v_fma_mixlo_f16 v22, v9, s8, 0
	v_pk_fma_f32 v[10:11], v[10:11], s[8:9], v[14:15] op_sel_hi:[1,0,1] neg_lo:[0,0,1] neg_hi:[0,0,1]
	v_lshl_add_u64 v[6:7], v[6:7], 0, v[0:1]
	v_lshl_add_u64 v[0:1], v[2:3], 0, v[0:1]
	v_fma_mixhi_f16 v8, v9, s8, -v22 op_sel_hi:[0,0,1]
	v_cvt_pk_f16_f32 v9, v10, v11
	global_store_dwordx2 v[6:7], v[16:17], off sc1
	global_store_dwordx2 v[6:7], v[18:19], off offset:512 sc1
	global_store_dwordx2 v[0:1], v[4:5], off sc1
	global_store_dwordx2 v[0:1], v[8:9], off offset:512 sc1
	s_endpgm
	s_endpgm
	s_endpgm
	s_endpgm
	s_endpgm
	s_endpgm
	s_endpgm
	s_endpgm
	s_endpgm
	s_endpgm
	s_endpgm
	s_endpgm
	s_endpgm
	s_endpgm
	s_endpgm
	s_endpgm
	s_endpgm
	s_endpgm
	s_endpgm
	s_endpgm
	s_endpgm
	s_endpgm
	s_endpgm
	s_endpgm
	s_endpgm
	s_endpgm
	s_endpgm
	s_endpgm
	s_endpgm
	s_endpgm
	s_endpgm
	s_endpgm
	s_endpgm
	s_endpgm
	s_endpgm
	s_endpgm
	s_endpgm
	s_endpgm
	s_endpgm
	s_endpgm
	s_endpgm
	s_endpgm
	s_endpgm
	s_endpgm
	s_endpgm
	s_endpgm
	s_endpgm
	s_endpgm
	s_endpgm
	s_endpgm
	s_endpgm
	s_endpgm
	s_endpgm
	s_endpgm

.LBB21_3:
	s_load_dwordx2 s[2:3], s[0:1], 0x58
	s_load_dwordx4 s[4:7], s[0:1], 0x48
	s_load_dwordx2 s[14:15], s[0:1], 0x0
	s_load_dwordx2 s[18:19], s[0:1], 0x18
	s_load_dwordx2 s[0:1], s[0:1], 0x8
	s_andn2_b64 vcc, exec, s[20:21]
	s_cbranch_vccnz .LBB21_5
	s_abs_i32 s13, s12
	v_cvt_f32_u32_e32 v1, s13
	s_sub_i32 s20, 0, s13
	v_sub_u32_e32 v5, 0, v2
	v_max_i32_e32 v5, v2, v5
	v_rcp_iflag_f32_e32 v1, v1
	v_xor_b32_e32 v4, s12, v2
	v_ashrrev_i32_e32 v4, 31, v4
	v_mul_f32_e32 v1, 0x4f7ffffe, v1
	v_cvt_u32_f32_e32 v1, v1
	v_mul_lo_u32 v6, s20, v1
	v_mul_hi_u32 v6, v1, v6
	v_add_u32_e32 v1, v1, v6
	v_mul_hi_u32 v1, v5, v1
	v_mul_lo_u32 v6, v1, s13
	v_sub_u32_e32 v5, v5, v6
	v_add_u32_e32 v7, 1, v1
	v_cmp_le_u32_e32 vcc, s13, v5
	v_subrev_u32_e32 v6, s13, v5
	s_nop 0
	v_cndmask_b32_e32 v1, v1, v7, vcc
	v_cndmask_b32_e32 v5, v5, v6, vcc
	v_add_u32_e32 v6, 1, v1
	v_cmp_le_u32_e32 vcc, s13, v5
	s_nop 1
	v_cndmask_b32_e32 v1, v1, v6, vcc
	v_xor_b32_e32 v1, v1, v4
	v_sub_u32_e32 v1, v1, v4
	v_mul_lo_u32 v4, v1, s12
	v_sub_u32_e32 v4, v2, v4
	v_ashrrev_i32_e32 v5, 31, v4
	v_mad_i64_i32 v[4:5], s[12:13], v1, 17, v[4:5]
.LBB21_5:
	v_lshlrev_b32_e32 v0, 2, v0
	v_and_b32_e32 v58, 0xfc, v0
	v_lshlrev_b64 v[4:5], 11, v[4:5]
	v_lshlrev_b32_e32 v0, 2, v58
	v_mov_b32_e32 v1, 0
	s_waitcnt lgkmcnt(0)
	v_lshl_add_u64 v[4:5], s[18:19], 0, v[4:5]
	v_lshl_add_u64 v[20:21], v[4:5], 0, v[0:1]
	global_load_dwordx4 v[4:7], v[20:21], off
	global_load_dwordx4 v[8:11], v0, s[16:17]
	global_load_dwordx4 v[12:15], v0, s[16:17] offset:1024
	global_load_dwordx4 v[16:19], v[20:21], off offset:1024
	v_lshlrev_b64 v[52:53], 11, v[2:3]
	v_lshl_add_u64 v[28:29], s[14:15], 0, v[52:53]
	v_lshl_add_u64 v[24:25], v[28:29], 0, v[0:1]
	v_mov_b32_e32 v59, 0x3727c5ac
	s_waitcnt lgkmcnt(0)
	v_lshl_add_u64 v[20:21], s[0:1], 2, v[28:29]
	v_lshl_add_u64 v[26:27], s[0:1], 3, v[28:29]
	v_lshl_add_u64 v[36:37], v[20:21], 0, v[0:1]
	global_load_dwordx4 v[20:23], v[24:25], off
	v_lshl_add_u64 v[40:41], v[26:27], 0, v[0:1]
	global_load_dwordx4 v[24:27], v[24:25], off offset:1024
	v_mad_u64_u32 v[44:45], s[12:13], s0, 12, v[28:29]
	v_mov_b32_e32 v38, v45
	v_mad_u64_u32 v[42:43], s[0:1], s1, 12, v[38:39]
	global_load_dwordx4 v[28:31], v[36:37], off
	global_load_dwordx4 v[32:35], v[36:37], off offset:1024
	v_mov_b32_e32 v45, v42
	global_load_dwordx4 v[36:39], v[40:41], off
	v_lshl_add_u64 v[54:55], v[44:45], 0, v[0:1]
	global_load_dwordx4 v[40:43], v[40:41], off offset:1024
	s_nop 0
	global_load_dwordx4 v[44:47], v[54:55], off
	global_load_dwordx4 v[48:51], v[54:55], off offset:1024
	v_mov_b32_e32 v60, 0x260
	v_lshlrev_b64 v[2:3], 10, v[2:3]
	s_waitcnt vmcnt(10)
	v_pk_add_f32 v[54:55], v[8:9], v[4:5]
	v_pk_add_f32 v[56:57], v[10:11], v[6:7]
	global_load_dwordx4 v[4:7], v0, s[8:9]
	global_load_dwordx4 v[8:11], v0, s[8:9] offset:1024
	s_waitcnt vmcnt(10)
	v_pk_add_f32 v[16:17], v[12:13], v[16:17]
	v_lshl_add_u64 v[12:13], s[4:5], 0, v[52:53]
	v_pk_add_f32 v[18:19], v[14:15], v[18:19]
	v_lshl_add_u64 v[52:53], v[12:13], 0, v[0:1]
	global_load_dwordx4 v[12:15], v0, s[10:11]
	s_mov_b32 s9, 0xf800000
	s_mov_b32 s8, 0x43000000
	s_waitcnt vmcnt(10)
	v_pk_add_f32 v[20:21], v[54:55], v[20:21]
	v_pk_add_f32 v[22:23], v[56:57], v[22:23]
	s_waitcnt vmcnt(9)
	v_pk_add_f32 v[24:25], v[16:17], v[24:25]
	v_pk_add_f32 v[26:27], v[18:19], v[26:27]
	global_load_dwordx4 v[16:19], v0, s[10:11] offset:1024
	s_waitcnt vmcnt(9)
	v_pk_add_f32 v[20:21], v[20:21], v[28:29]
	v_pk_add_f32 v[22:23], v[22:23], v[30:31]
	s_waitcnt vmcnt(8)
	v_pk_add_f32 v[24:25], v[24:25], v[32:33]
	s_waitcnt vmcnt(7)
	v_pk_add_f32 v[20:21], v[20:21], v[36:37]
	v_pk_add_f32 v[22:23], v[22:23], v[38:39]
	s_waitcnt vmcnt(5)
	v_pk_add_f32 v[20:21], v[20:21], v[44:45]
	v_pk_add_f32 v[22:23], v[22:23], v[46:47]
	v_add_f32_e32 v0, 0, v20
	v_add_f32_e32 v0, v0, v21
	v_pk_add_f32 v[24:25], v[24:25], v[40:41]
	v_add_f32_e32 v0, v0, v22
	v_pk_add_f32 v[26:27], v[26:27], v[34:35]
	s_waitcnt vmcnt(4)
	v_pk_add_f32 v[24:25], v[24:25], v[48:49]
	v_add_f32_e32 v0, v0, v23
	v_pk_add_f32 v[26:27], v[26:27], v[42:43]
	v_add_f32_e32 v0, v0, v24
	v_pk_add_f32 v[26:27], v[26:27], v[50:51]
	v_add_f32_e32 v0, v0, v25
	v_add_f32_e32 v0, v0, v26
	v_add_f32_e32 v0, v0, v27
	s_nop 1
	v_add_f32_dpp v0, v0, v0 quad_perm:[1,0,3,2] row_mask:0xf bank_mask:0xf bound_ctrl:1
	s_nop 1
	v_add_f32_dpp v0, v0, v0 quad_perm:[2,3,0,1] row_mask:0xf bank_mask:0xf bound_ctrl:1
	s_nop 1
	v_add_f32_dpp v0, v0, v0 row_half_mirror row_mask:0xf bank_mask:0xf bound_ctrl:1
	s_nop 1
	v_add_f32_dpp v0, v0, v0 row_mirror row_mask:0xf bank_mask:0xf bound_ctrl:1
	s_nop 0
	v_readlane_b32 s4, v0, 16
	v_readlane_b32 s5, v0, 48
	v_readlane_b32 s0, v0, 0
	v_readlane_b32 s1, v0, 32
	v_mov_b32_e32 v28, s4
	v_mov_b32_e32 v29, s5
	v_pk_add_f32 v[28:29], s[0:1], v[28:29]
	s_nop 0
	v_add_f32_e32 v0, v28, v29
	v_mul_f32_e32 v0, 0x3b000000, v0
	v_pk_add_f32 v[20:21], v[20:21], v[0:1] op_sel_hi:[1,0] neg_lo:[0,1] neg_hi:[0,1]
	v_pk_add_f32 v[22:23], v[22:23], v[0:1] op_sel_hi:[1,0] neg_lo:[0,1] neg_hi:[0,1]
	v_pk_mul_f32 v[28:29], v[20:21], v[20:21]
	v_pk_add_f32 v[24:25], v[24:25], v[0:1] op_sel_hi:[1,0] neg_lo:[0,1] neg_hi:[0,1]
	v_pk_add_f32 v[26:27], v[26:27], v[0:1] op_sel_hi:[1,0] neg_lo:[0,1] neg_hi:[0,1]
	v_pk_mul_f32 v[30:31], v[22:23], v[22:23]
	v_add_f32_e32 v0, v28, v29
	v_add_f32_e32 v0, v0, v30
	v_pk_mul_f32 v[32:33], v[24:25], v[24:25]
	v_add_f32_e32 v0, v0, v31
	v_add_f32_e32 v0, v0, v32
	v_pk_mul_f32 v[34:35], v[26:27], v[26:27]
	v_add_f32_e32 v0, v0, v33
	v_add_f32_e32 v0, v0, v34
	v_add_f32_e32 v0, v0, v35
	s_waitcnt vmcnt(3)
	v_pk_mul_f32 v[4:5], v[4:5], v[20:21]
	v_add_f32_dpp v0, v0, v0 quad_perm:[1,0,3,2] row_mask:0xf bank_mask:0xf bound_ctrl:1
	v_pk_mul_f32 v[6:7], v[6:7], v[22:23]
	s_waitcnt vmcnt(2)
	v_pk_mul_f32 v[8:9], v[8:9], v[24:25]
	v_add_f32_dpp v0, v0, v0 quad_perm:[2,3,0,1] row_mask:0xf bank_mask:0xf bound_ctrl:1
	v_pk_mul_f32 v[10:11], v[10:11], v[26:27]
	s_nop 0
	v_add_f32_dpp v0, v0, v0 row_half_mirror row_mask:0xf bank_mask:0xf bound_ctrl:1
	s_nop 1
	v_add_f32_dpp v0, v0, v0 row_mirror row_mask:0xf bank_mask:0xf bound_ctrl:1
	s_nop 0
	v_readlane_b32 s4, v0, 16
	v_readlane_b32 s5, v0, 48
	v_readlane_b32 s0, v0, 0
	v_readlane_b32 s1, v0, 32
	v_mov_b32_e32 v28, s4
	v_mov_b32_e32 v29, s5
	v_pk_add_f32 v[28:29], s[0:1], v[28:29]
	s_nop 0
	v_add_f32_e32 v0, v28, v29
	v_fmac_f32_e32 v59, 0x3b000000, v0
	v_mul_f32_e32 v0, 0x4f800000, v59
	v_cmp_gt_f32_e32 vcc, s9, v59
	s_nop 1
	v_cndmask_b32_e32 v0, v59, v0, vcc
	v_sqrt_f32_e32 v28, v0
	s_nop 0
	v_add_u32_e32 v20, -1, v28
	v_add_u32_e32 v21, 1, v28
	v_fma_f32 v22, -v20, v28, v0
	v_fma_f32 v23, -v21, v28, v0
	v_cmp_ge_f32_e64 s[0:1], 0, v22
	s_nop 1
	v_cndmask_b32_e64 v20, v28, v20, s[0:1]
	v_cmp_lt_f32_e64 s[0:1], 0, v23
	s_nop 1
	v_cndmask_b32_e64 v20, v20, v21, s[0:1]
	v_mul_f32_e32 v21, 0x37800000, v20
	v_cndmask_b32_e32 v20, v20, v21, vcc
	v_cmp_class_f32_e32 vcc, v0, v60
	s_nop 1
	v_cndmask_b32_e32 v0, v20, v0, vcc
	v_div_scale_f32 v20, s[0:1], v0, v0, 1.0
	v_rcp_f32_e32 v21, v20
	v_div_scale_f32 v22, vcc, 1.0, v0, 1.0
	v_fma_f32 v23, -v20, v21, 1.0
	v_fmac_f32_e32 v21, v23, v21
	v_mul_f32_e32 v23, v22, v21
	v_fma_f32 v24, -v20, v23, v22
	v_fmac_f32_e32 v23, v24, v21
	v_fma_f32 v20, -v20, v23, v22
	v_div_fmas_f32 v20, v20, v21, v23
	v_div_fixup_f32 v0, v20, v0, 1.0
	s_waitcnt vmcnt(1)
	v_pk_fma_f32 v[4:5], v[0:1], v[4:5], v[12:13] op_sel_hi:[0,1,1]
	v_pk_fma_f32 v[6:7], v[0:1], v[6:7], v[14:15] op_sel_hi:[0,1,1]
	s_waitcnt vmcnt(0)
	v_pk_fma_f32 v[8:9], v[0:1], v[8:9], v[16:17] op_sel_hi:[0,1,1]
	v_fma_mixlo_f16 v12, v4, s8, 0
	v_pk_fma_f32 v[10:11], v[0:1], v[10:11], v[18:19] op_sel_hi:[0,1,1]
	global_store_dwordx4 v[52:53], v[4:7], off sc1
	global_store_dwordx4 v[52:53], v[8:11], off offset:1024 sc1
	v_mul_f32_e32 v0, 0x43000000, v4
	v_fma_mixlo_f16 v4, v4, s8, -v12 op_sel_hi:[0,0,1]
	v_fma_mixlo_f16 v12, v8, s8, 0
	v_mul_f32_e32 v13, 0x43000000, v8
	v_fma_mixlo_f16 v8, v8, s8, -v12 op_sel_hi:[0,0,1]
	v_mul_f32_e32 v12, 0x43000000, v5
	v_fma_mixlo_f16 v14, v5, s8, 0
	v_cvt_pk_f16_f32 v12, v0, v12
	v_mul_f32_e32 v0, 0x43000000, v9
	v_pk_mul_f32 v[16:17], v[6:7], s[8:9] op_sel_hi:[1,0]
	v_fma_mixhi_f16 v4, v5, s8, -v14 op_sel_hi:[0,0,1]
	v_cvt_pk_f16_f32 v14, v13, v0
	v_cvt_pk_f16_f32 v13, v16, v17
	v_pk_mul_f32 v[18:19], v[10:11], s[8:9] op_sel_hi:[1,0]
	v_cvt_f32_f16_e32 v16, v13
	v_cvt_f32_f16_sdwa v17, v13 dst_sel:DWORD dst_unused:UNUSED_PAD src0_sel:WORD_1
	v_cvt_pk_f16_f32 v15, v18, v19
	v_cvt_f32_f16_e32 v18, v15
	v_cvt_f32_f16_sdwa v19, v15 dst_sel:DWORD dst_unused:UNUSED_PAD src0_sel:WORD_1
	v_fma_mixlo_f16 v5, v9, s8, 0
	v_pk_fma_f32 v[6:7], v[6:7], s[8:9], v[16:17] op_sel_hi:[1,0,1] neg_lo:[0,0,1] neg_hi:[0,0,1]
	v_fma_mixhi_f16 v8, v9, s8, -v5 op_sel_hi:[0,0,1]
	v_cvt_pk_f16_f32 v5, v6, v7
	v_pk_fma_f32 v[6:7], v[10:11], s[8:9], v[18:19] op_sel_hi:[1,0,1] neg_lo:[0,0,1] neg_hi:[0,0,1]
	v_lshlrev_b32_e32 v0, 1, v58
	v_cvt_pk_f16_f32 v9, v6, v7
	v_lshl_add_u64 v[6:7], s[6:7], 0, v[2:3]
	v_lshl_add_u64 v[2:3], s[2:3], 0, v[2:3]
	v_lshl_add_u64 v[6:7], v[6:7], 0, v[0:1]
	v_lshl_add_u64 v[0:1], v[2:3], 0, v[0:1]
	global_store_dwordx2 v[6:7], v[12:13], off sc1
	global_store_dwordx2 v[6:7], v[14:15], off offset:512 sc1
	global_store_dwordx2 v[0:1], v[4:5], off sc1
	global_store_dwordx2 v[0:1], v[8:9], off offset:512 sc1
	s_endpgm
	s_endpgm
	s_endpgm
	s_endpgm
	s_endpgm
	s_endpgm
	s_endpgm
	s_endpgm
	s_endpgm
	s_endpgm
	s_endpgm
	s_endpgm
	s_endpgm

.LBB22_5:
	v_lshlrev_b32_e32 v0, 2, v0
	v_and_b32_e32 v66, 0xfc, v0
	v_lshlrev_b64 v[4:5], 11, v[4:5]
	v_lshlrev_b32_e32 v0, 2, v66
	v_mov_b32_e32 v1, 0
	s_waitcnt lgkmcnt(0)
	v_lshl_add_u64 v[4:5], s[18:19], 0, v[4:5]
	v_lshl_add_u64 v[20:21], v[4:5], 0, v[0:1]
	global_load_dwordx4 v[4:7], v[20:21], off
	global_load_dwordx4 v[8:11], v0, s[16:17]
	global_load_dwordx4 v[12:15], v0, s[16:17] offset:1024
	global_load_dwordx4 v[16:19], v[20:21], off offset:1024
	v_lshlrev_b64 v[48:49], 11, v[2:3]
	v_lshl_add_u64 v[40:41], s[14:15], 0, v[48:49]
	v_lshl_add_u64 v[28:29], v[40:41], 0, v[0:1]
	global_load_dwordx4 v[20:23], v[28:29], off
	global_load_dwordx4 v[24:27], v[28:29], off offset:1024
	v_lshlrev_b64 v[2:3], 10, v[2:3]
	s_waitcnt lgkmcnt(0)
	v_lshl_add_u64 v[28:29], s[0:1], 2, v[40:41]
	v_lshl_add_u64 v[42:43], v[28:29], 0, v[0:1]
	v_mad_u64_u32 v[36:37], s[12:13], s0, 12, v[40:41]
	v_lshl_add_u64 v[32:33], s[0:1], 3, v[40:41]
	global_load_dwordx4 v[28:31], v[42:43], off
	v_mov_b32_e32 v38, v37
	v_lshl_add_u64 v[44:45], v[32:33], 0, v[0:1]
	v_mad_u64_u32 v[38:39], s[12:13], s1, 12, v[38:39]
	global_load_dwordx4 v[32:35], v[44:45], off
	v_mov_b32_e32 v37, v38
	v_lshl_add_u64 v[46:47], v[36:37], 0, v[0:1]
	global_load_dwordx4 v[36:39], v[46:47], off
	v_mad_u64_u32 v[52:53], s[12:13], s0, 20, v[40:41]
	v_mad_u64_u32 v[54:55], s[12:13], s0, 24, v[40:41]
	v_lshl_add_u64 v[50:51], s[0:1], 4, v[40:41]
	v_mad_u64_u32 v[40:41], s[12:13], s0, 28, v[40:41]
	v_lshl_add_u64 v[50:51], v[50:51], 0, v[0:1]
	s_waitcnt vmcnt(7)
	v_pk_add_f32 v[56:57], v[8:9], v[4:5]
	v_mov_b32_e32 v4, v53
	v_pk_add_f32 v[58:59], v[10:11], v[6:7]
	v_mov_b32_e32 v6, v55
	v_mad_u64_u32 v[10:11], s[12:13], s1, 20, v[4:5]
	s_waitcnt vmcnt(5)
	v_pk_add_f32 v[60:61], v[12:13], v[16:17]
	v_mov_b32_e32 v8, v41
	v_mad_u64_u32 v[12:13], s[12:13], s1, 24, v[6:7]
	v_mov_b32_e32 v53, v10
	v_pk_add_f32 v[62:63], v[14:15], v[18:19]
	v_mad_u64_u32 v[14:15], s[0:1], s1, 28, v[8:9]
	global_load_dwordx4 v[4:7], v[50:51], off
	v_mov_b32_e32 v55, v12
	v_lshl_add_u64 v[52:53], v[52:53], 0, v[0:1]
	v_mov_b32_e32 v41, v14
	v_lshl_add_u64 v[54:55], v[54:55], 0, v[0:1]
	global_load_dwordx4 v[12:15], v[52:53], off
	v_lshl_add_u64 v[64:65], v[40:41], 0, v[0:1]
	global_load_dwordx4 v[16:19], v[54:55], off
	global_load_dwordx4 v[8:11], v[42:43], off offset:1024
	s_waitcnt vmcnt(8)
	v_pk_add_f32 v[40:41], v[56:57], v[20:21]
	v_pk_add_f32 v[42:43], v[58:59], v[22:23]
	global_load_dwordx4 v[20:23], v[64:65], off
	s_waitcnt vmcnt(8)
	v_pk_add_f32 v[56:57], v[60:61], v[24:25]
	v_pk_add_f32 v[58:59], v[62:63], v[26:27]
	s_waitcnt vmcnt(7)
	v_pk_add_f32 v[40:41], v[40:41], v[28:29]
	v_pk_add_f32 v[42:43], v[42:43], v[30:31]
	global_load_dwordx4 v[24:27], v[44:45], off offset:1024
	global_load_dwordx4 v[28:31], v[46:47], off offset:1024
	s_waitcnt vmcnt(8)
	v_pk_add_f32 v[44:45], v[40:41], v[32:33]
	v_pk_add_f32 v[46:47], v[42:43], v[34:35]
	global_load_dwordx4 v[32:35], v[50:51], off offset:1024
	global_load_dwordx4 v[40:43], v[52:53], off offset:1024
	s_waitcnt vmcnt(9)
	v_pk_add_f32 v[50:51], v[44:45], v[36:37]
	v_pk_add_f32 v[52:53], v[46:47], v[38:39]
	global_load_dwordx4 v[36:39], v[54:55], off offset:1024
	global_load_dwordx4 v[44:47], v[64:65], off offset:1024
	s_waitcnt vmcnt(10)
	v_pk_add_f32 v[4:5], v[50:51], v[4:5]
	v_pk_add_f32 v[6:7], v[52:53], v[6:7]
	s_waitcnt vmcnt(9)
	v_pk_add_f32 v[50:51], v[4:5], v[12:13]
	v_pk_add_f32 v[52:53], v[6:7], v[14:15]
	global_load_dwordx4 v[4:7], v0, s[8:9]
	global_load_dwordx4 v[12:15], v0, s[10:11]
	s_waitcnt vmcnt(10)
	v_pk_add_f32 v[16:17], v[50:51], v[16:17]
	v_pk_add_f32 v[18:19], v[52:53], v[18:19]
	s_waitcnt vmcnt(9)
	v_pk_add_f32 v[8:9], v[56:57], v[8:9]
	s_waitcnt vmcnt(8)
	v_pk_add_f32 v[50:51], v[16:17], v[20:21]
	v_pk_add_f32 v[52:53], v[18:19], v[22:23]
	global_load_dwordx4 v[16:19], v0, s[8:9] offset:1024
	global_load_dwordx4 v[20:23], v0, s[10:11] offset:1024
	v_pk_add_f32 v[10:11], v[58:59], v[10:11]
	s_waitcnt vmcnt(9)
	v_pk_add_f32 v[8:9], v[8:9], v[24:25]
	v_add_f32_e32 v24, 0, v50
	s_waitcnt vmcnt(8)
	v_pk_add_f32 v[8:9], v[8:9], v[28:29]
	v_pk_add_f32 v[10:11], v[10:11], v[26:27]
	s_waitcnt vmcnt(7)
	v_pk_add_f32 v[8:9], v[8:9], v[32:33]
	v_add_f32_e32 v24, v24, v51
	s_waitcnt vmcnt(6)
	v_pk_add_f32 v[8:9], v[8:9], v[40:41]
	v_pk_add_f32 v[10:11], v[10:11], v[30:31]
	v_add_f32_e32 v24, v24, v52
	s_waitcnt vmcnt(5)
	v_pk_add_f32 v[8:9], v[8:9], v[36:37]
	v_pk_add_f32 v[10:11], v[10:11], v[34:35]
	v_add_f32_e32 v24, v24, v53
	s_waitcnt vmcnt(4)
	v_pk_add_f32 v[8:9], v[8:9], v[44:45]
	v_pk_add_f32 v[10:11], v[10:11], v[42:43]
	v_add_f32_e32 v24, v24, v8
	v_pk_add_f32 v[10:11], v[10:11], v[38:39]
	v_add_f32_e32 v24, v24, v9
	v_pk_add_f32 v[10:11], v[10:11], v[46:47]
	s_nop 0
	v_add_f32_e32 v24, v24, v10
	v_add_f32_e32 v24, v24, v11
	s_nop 1
	v_add_f32_dpp v24, v24, v24 quad_perm:[1,0,3,2] row_mask:0xf bank_mask:0xf bound_ctrl:1
	s_nop 1
	v_add_f32_dpp v24, v24, v24 quad_perm:[2,3,0,1] row_mask:0xf bank_mask:0xf bound_ctrl:1
	s_nop 1
	v_add_f32_dpp v24, v24, v24 row_half_mirror row_mask:0xf bank_mask:0xf bound_ctrl:1
	s_nop 1
	v_add_f32_dpp v24, v24, v24 row_mirror row_mask:0xf bank_mask:0xf bound_ctrl:1
	s_nop 0
	v_readlane_b32 s8, v24, 16
	v_readlane_b32 s9, v24, 48
	v_readlane_b32 s0, v24, 0
	v_readlane_b32 s1, v24, 32
	v_mov_b32_e32 v24, s8
	v_mov_b32_e32 v25, s9
	v_pk_add_f32 v[24:25], s[0:1], v[24:25]
	s_nop 0
	v_add_f32_e32 v24, v24, v25
	v_mul_f32_e32 v24, 0x3b000000, v24
	v_pk_add_f32 v[26:27], v[50:51], v[24:25] op_sel_hi:[1,0] neg_lo:[0,1] neg_hi:[0,1]
	v_pk_add_f32 v[30:31], v[52:53], v[24:25] op_sel_hi:[1,0] neg_lo:[0,1] neg_hi:[0,1]
	v_pk_mul_f32 v[28:29], v[26:27], v[26:27]
	v_pk_mul_f32 v[32:33], v[30:31], v[30:31]
	v_add_f32_e32 v28, v28, v29
	v_pk_add_f32 v[8:9], v[8:9], v[24:25] op_sel_hi:[1,0] neg_lo:[0,1] neg_hi:[0,1]
	v_add_f32_e32 v28, v28, v32
	v_pk_mul_f32 v[34:35], v[8:9], v[8:9]
	v_add_f32_e32 v28, v28, v33
	v_pk_add_f32 v[10:11], v[10:11], v[24:25] op_sel_hi:[1,0] neg_lo:[0,1] neg_hi:[0,1]
	v_add_f32_e32 v28, v28, v34
	v_pk_mul_f32 v[24:25], v[10:11], v[10:11]
	v_add_f32_e32 v28, v28, v35
	v_add_f32_e32 v24, v28, v24
	v_add_f32_e32 v24, v24, v25
	s_waitcnt vmcnt(3)
	v_pk_mul_f32 v[4:5], v[4:5], v[26:27]
	v_add_f32_dpp v24, v24, v24 quad_perm:[1,0,3,2] row_mask:0xf bank_mask:0xf bound_ctrl:1
	v_pk_mul_f32 v[6:7], v[6:7], v[30:31]
	s_waitcnt vmcnt(1)
	v_pk_mul_f32 v[8:9], v[16:17], v[8:9]
	v_add_f32_dpp v24, v24, v24 quad_perm:[2,3,0,1] row_mask:0xf bank_mask:0xf bound_ctrl:1
	v_pk_mul_f32 v[10:11], v[18:19], v[10:11]
	s_nop 0
	v_add_f32_dpp v24, v24, v24 row_half_mirror row_mask:0xf bank_mask:0xf bound_ctrl:1
	s_nop 1
	v_add_f32_dpp v24, v24, v24 row_mirror row_mask:0xf bank_mask:0xf bound_ctrl:1
	s_nop 0
	v_readlane_b32 s8, v24, 16
	v_readlane_b32 s9, v24, 48
	v_readlane_b32 s0, v24, 0
	v_readlane_b32 s1, v24, 32
	v_mov_b32_e32 v24, s8
	v_mov_b32_e32 v25, s9
	v_pk_add_f32 v[24:25], s[0:1], v[24:25]
	s_mov_b32 s0, 0xf800000
	v_add_f32_e32 v24, v24, v25
	v_mov_b32_e32 v25, 0x3727c5ac
	v_fmac_f32_e32 v25, 0x3b000000, v24
	v_mul_f32_e32 v24, 0x4f800000, v25
	v_cmp_gt_f32_e32 vcc, s0, v25
	s_nop 1
	v_cndmask_b32_e32 v24, v25, v24, vcc
	v_sqrt_f32_e32 v25, v24
	s_nop 0
	v_add_u32_e32 v28, -1, v25
	v_fma_f32 v29, -v28, v25, v24
	v_cmp_ge_f32_e64 s[0:1], 0, v29
	v_add_u32_e32 v29, 1, v25
	s_nop 0
	v_cndmask_b32_e64 v28, v25, v28, s[0:1]
	v_fma_f32 v25, -v29, v25, v24
	v_cmp_lt_f32_e64 s[0:1], 0, v25
	s_nop 1
	v_cndmask_b32_e64 v25, v28, v29, s[0:1]
	v_mul_f32_e32 v28, 0x37800000, v25
	v_cndmask_b32_e32 v25, v25, v28, vcc
	v_mov_b32_e32 v28, 0x260
	v_cmp_class_f32_e32 vcc, v24, v28
	s_nop 1
	v_cndmask_b32_e32 v28, v25, v24, vcc
	v_div_scale_f32 v29, s[0:1], v28, v28, 1.0
	v_rcp_f32_e32 v32, v29
	v_lshl_add_u64 v[24:25], s[4:5], 0, v[48:49]
	v_lshl_add_u64 v[24:25], v[24:25], 0, v[0:1]
	s_mov_b32 s0, 0x43000000
	v_fma_f32 v0, -v29, v32, 1.0
	v_fmac_f32_e32 v32, v0, v32
	v_div_scale_f32 v0, vcc, 1.0, v28, 1.0
	v_mul_f32_e32 v33, v0, v32
	v_fma_f32 v34, -v29, v33, v0
	v_fmac_f32_e32 v33, v34, v32
	v_fma_f32 v0, -v29, v33, v0
	v_div_fmas_f32 v0, v0, v32, v33
	v_div_fixup_f32 v0, v0, v28, 1.0
	v_pk_fma_f32 v[4:5], v[0:1], v[4:5], v[12:13] op_sel_hi:[0,1,1]
	v_pk_fma_f32 v[6:7], v[0:1], v[6:7], v[14:15] op_sel_hi:[0,1,1]
	s_waitcnt vmcnt(0)
	v_pk_fma_f32 v[8:9], v[0:1], v[8:9], v[20:21] op_sel_hi:[0,1,1]
	v_fma_mixlo_f16 v12, v4, s0, 0
	v_pk_fma_f32 v[10:11], v[0:1], v[10:11], v[22:23] op_sel_hi:[0,1,1]
	global_store_dwordx4 v[24:25], v[4:7], off sc1
	global_store_dwordx4 v[24:25], v[8:11], off offset:1024 sc1
	v_mul_f32_e32 v0, 0x43000000, v4
	v_fma_mixlo_f16 v4, v4, s0, -v12 op_sel_hi:[0,0,1]
	v_fma_mixlo_f16 v12, v8, s0, 0
	v_mul_f32_e32 v13, 0x43000000, v8
	v_fma_mixlo_f16 v8, v8, s0, -v12 op_sel_hi:[0,0,1]
	v_mul_f32_e32 v12, 0x43000000, v5
	v_fma_mixlo_f16 v14, v5, s0, 0
	v_cvt_pk_f16_f32 v12, v0, v12
	v_mul_f32_e32 v0, 0x43000000, v9
	v_pk_mul_f32 v[16:17], v[6:7], s[0:1] op_sel_hi:[1,0]
	v_fma_mixhi_f16 v4, v5, s0, -v14 op_sel_hi:[0,0,1]
	v_cvt_pk_f16_f32 v14, v13, v0
	v_cvt_pk_f16_f32 v13, v16, v17
	v_pk_mul_f32 v[18:19], v[10:11], s[0:1] op_sel_hi:[1,0]
	v_cvt_f32_f16_e32 v16, v13
	v_cvt_f32_f16_sdwa v17, v13 dst_sel:DWORD dst_unused:UNUSED_PAD src0_sel:WORD_1
	v_cvt_pk_f16_f32 v15, v18, v19
	v_cvt_f32_f16_e32 v18, v15
	v_cvt_f32_f16_sdwa v19, v15 dst_sel:DWORD dst_unused:UNUSED_PAD src0_sel:WORD_1
	v_fma_mixlo_f16 v5, v9, s0, 0
	v_pk_fma_f32 v[6:7], v[6:7], s[0:1], v[16:17] op_sel_hi:[1,0,1] neg_lo:[0,0,1] neg_hi:[0,0,1]
	v_fma_mixhi_f16 v8, v9, s0, -v5 op_sel_hi:[0,0,1]
	v_cvt_pk_f16_f32 v5, v6, v7
	v_pk_fma_f32 v[6:7], v[10:11], s[0:1], v[18:19] op_sel_hi:[1,0,1] neg_lo:[0,0,1] neg_hi:[0,0,1]
	v_lshlrev_b32_e32 v0, 1, v66
	v_cvt_pk_f16_f32 v9, v6, v7
	v_lshl_add_u64 v[6:7], s[6:7], 0, v[2:3]
	v_lshl_add_u64 v[2:3], s[2:3], 0, v[2:3]
	v_lshl_add_u64 v[6:7], v[6:7], 0, v[0:1]
	v_lshl_add_u64 v[0:1], v[2:3], 0, v[0:1]
	global_store_dwordx2 v[6:7], v[12:13], off sc1
	global_store_dwordx2 v[6:7], v[14:15], off offset:512 sc1
	global_store_dwordx2 v[0:1], v[4:5], off sc1
	global_store_dwordx2 v[0:1], v[8:9], off offset:512 sc1
	s_endpgm
	s_endpgm
	s_endpgm
	s_endpgm
	s_endpgm
	s_endpgm
	s_endpgm
	s_endpgm
	s_endpgm
	s_endpgm
	s_endpgm
	s_endpgm
	s_endpgm
	s_endpgm
	s_endpgm
	s_endpgm
	s_endpgm
	s_endpgm
	s_endpgm
	s_endpgm
	s_endpgm
	s_endpgm
	s_endpgm
	s_endpgm
	s_endpgm
	s_endpgm
	s_endpgm
	s_endpgm
	s_endpgm
	s_endpgm
	s_endpgm
	s_endpgm
	s_endpgm
	s_endpgm
	s_endpgm
	s_endpgm
	s_endpgm
	s_endpgm
	s_endpgm
	s_endpgm
	s_endpgm
	s_endpgm
	s_endpgm
	s_endpgm
	s_endpgm
	s_endpgm
	s_endpgm
	s_endpgm
	s_endpgm
	s_endpgm
	s_endpgm
	s_endpgm
	s_endpgm
	s_endpgm
	s_endpgm
	s_endpgm
	s_endpgm
	s_endpgm
